# speedup vs baseline: 1.0143x; 1.0133x over previous
_Z7gat_prePKfS0_S0_PDF16_PfS2_:
	s_mov_b32 s2, s14
	s_load_dwordx8 s[32:39], s[0:1], 0x0
	s_load_dwordx4 s[40:43], s[0:1], 0x20
	s_waitcnt lgkmcnt(0)
	s_branch .Lpre_body
	s_nop 0
	s_nop 0
	s_nop 0
	s_nop 0
	s_nop 0
	s_nop 0
	s_nop 0
	s_nop 0
	s_nop 0
	s_nop 0
	s_nop 0
	s_nop 0
	s_nop 0
	s_nop 0
	s_nop 0
	s_nop 0
	s_nop 0
	s_nop 0
	s_nop 0
	s_nop 0
	s_nop 0
	s_nop 0
	s_nop 0
	s_nop 0
	s_nop 0
	s_nop 0
	s_nop 0
	s_nop 0
	s_nop 0
	s_nop 0
	s_nop 0
	s_nop 0
	s_nop 0
	s_nop 0
	s_nop 0
	s_nop 0
	s_nop 0
	s_nop 0
	s_nop 0
	s_nop 0
	s_nop 0
	s_nop 0
	s_nop 0
	s_nop 0
	s_nop 0
	s_nop 0
	s_nop 0
	s_nop 0
	s_nop 0
	s_nop 0
	s_nop 0
	s_nop 0
	s_nop 0
	s_nop 0
	s_nop 0
	s_nop 0
	s_nop 0
.Lpre_preloaded:
	s_mov_b64 s[32:33], s[2:3]
	s_mov_b64 s[34:35], s[4:5]
	s_mov_b64 s[36:37], s[6:7]
	s_mov_b64 s[38:39], s[8:9]
	s_mov_b64 s[40:41], s[10:11]
	s_mov_b64 s[42:43], s[12:13]
	s_mov_b32 s2, s14
.Lpre_body:
	s_mov_b64 s[8:9], s[36:37]
	s_mov_b64 s[4:5], s[32:33]
	s_mov_b64 s[6:7], s[34:35]
	v_and_b32_e32 v1, 3, v0
	v_lshlrev_b32_e32 v18, 6, v1
	v_mov_b32_e32 v19, 0
	s_waitcnt lgkmcnt(0)
	global_load_dwordx4 v[22:25], v18, s[8:9]
	v_lshrrev_b32_e32 v20, 2, v0
	v_lshlrev_b32_e32 v2, 8, v20
	v_mov_b32_e32 v3, v19
	v_lshl_add_u64 v[2:3], s[6:7], 0, v[2:3]
	v_lshl_add_u64 v[2:3], v[2:3], 0, v[18:19]
	global_load_dwordx4 v[26:29], v[2:3], off
	global_load_dwordx4 v[30:33], v18, s[8:9] offset:256
	global_load_dwordx4 v[34:37], v[2:3], off offset:16
	global_load_dwordx4 v[38:41], v[2:3], off offset:32
	global_load_dwordx4 v[42:45], v18, s[8:9] offset:16
	global_load_dwordx4 v[46:49], v18, s[8:9] offset:272
	global_load_dwordx4 v[50:53], v18, s[8:9] offset:32
	global_load_dwordx4 v[54:57], v18, s[8:9] offset:288
	global_load_dwordx4 v[58:61], v[2:3], off offset:48
	global_load_dwordx4 v[62:65], v18, s[8:9] offset:48
	global_load_dwordx4 v[66:69], v18, s[8:9] offset:304
	s_lshl_b32 s2, s2, 6
	s_ashr_i32 s3, s2, 31
	s_lshl_b64 s[8:9], s[2:3], 9
	s_add_u32 s4, s4, s8
	v_mul_u32_u24_e32 v2, 0x1100, v1
	s_addc_u32 s5, s5, s9
	v_lshlrev_b32_e32 v18, 4, v0
	s_movk_i32 s7, 0x2000
	v_lshl_or_b32 v76, v20, 1, v2
	v_lshl_add_u64 v[2:3], s[4:5], 0, v[18:19]
	v_add_co_u32_e32 v70, vcc, s7, v2
	s_movk_i32 s10, 0x4000
	s_nop 0
	v_addc_co_u32_e32 v71, vcc, 0, v3, vcc
	v_add_co_u32_e32 v72, vcc, s10, v2
	s_movk_i32 s11, 0x6000
	s_nop 0
	v_addc_co_u32_e32 v73, vcc, 0, v3, vcc
	v_add_co_u32_e32 v74, vcc, s11, v2
	v_readfirstlane_b32 s6, v0
	s_nop 0
	v_addc_co_u32_e32 v75, vcc, 0, v3, vcc
	global_load_dwordx4 v[10:13], v[70:71], off nt
	global_load_dwordx4 v[6:9], v[72:73], off nt
	global_load_dwordx4 v[14:17], v18, s[4:5] nt
	global_load_dwordx4 v[2:5], v[74:75], off nt
	s_waitcnt vmcnt(14)
	v_cvt_f16_f32_e32 v18, v26
	v_cvt_f16_f32_e32 v21, v27
	s_waitcnt vmcnt(12)
	v_cvt_f16_f32_e32 v70, v34
	v_cvt_f16_f32_e32 v71, v35
	v_fma_f32 v19, v26, v22, 0
	v_fmac_f32_e32 v19, v27, v23
	v_fmac_f32_e32 v19, v28, v24
	v_fma_f32 v22, v26, v30, 0
	v_cvt_f16_f32_e32 v26, v28
	v_fmac_f32_e32 v19, v29, v25
	v_cvt_f16_f32_e32 v30, v29
	v_fmac_f32_e32 v22, v27, v31
	s_waitcnt vmcnt(10)
	v_fmac_f32_e32 v19, v34, v42
	v_fmac_f32_e32 v22, v28, v32
	ds_write_b16 v76, v18 offset:51200
	ds_write_b16 v76, v21 offset:51472
	ds_write_b16 v76, v26 offset:51744
	ds_write_b16 v76, v30 offset:52016
	v_fmac_f32_e32 v19, v35, v43
	s_waitcnt vmcnt(6)
	v_cvt_f16_f32_e32 v18, v58
	v_fmac_f32_e32 v22, v29, v33
	v_fmac_f32_e32 v19, v36, v44
	v_cvt_f16_f32_e32 v72, v36
	v_fmac_f32_e32 v22, v34, v46
	v_fmac_f32_e32 v19, v37, v45
	v_cvt_f16_f32_e32 v73, v37
	v_fmac_f32_e32 v22, v35, v47
	v_fmac_f32_e32 v19, v38, v50
	v_cvt_f16_f32_e32 v74, v38
	v_cvt_f16_f32_e32 v75, v39
	v_cvt_f16_f32_e32 v77, v40
	ds_write_b16 v76, v70 offset:52288
	ds_write_b16 v76, v71 offset:52560
	ds_write_b16 v76, v72 offset:52832
	ds_write_b16 v76, v73 offset:53104
	ds_write_b16 v76, v74 offset:53376
	ds_write_b16 v76, v75 offset:53648
	ds_write_b16 v76, v77 offset:53920
	v_fmac_f32_e32 v22, v36, v48
	v_fmac_f32_e32 v19, v39, v51
	ds_write_b16 v76, v18 offset:54464
	v_mbcnt_lo_u32_b32 v18, -1, 0
	v_fmac_f32_e32 v22, v37, v49
	v_fmac_f32_e32 v19, v40, v52
	v_mbcnt_hi_u32_b32 v23, -1, v18
	v_fmac_f32_e32 v22, v38, v54
	v_fmac_f32_e32 v19, v41, v53
	v_and_b32_e32 v21, 64, v23
	v_fmac_f32_e32 v22, v39, v55
	s_waitcnt vmcnt(5)
	v_fmac_f32_e32 v19, v58, v62
	v_xor_b32_e32 v18, 1, v23
	v_add_u32_e32 v24, 64, v21
	v_fmac_f32_e32 v22, v40, v56
	v_fmac_f32_e32 v19, v59, v63
	v_cmp_lt_i32_e32 vcc, v18, v24
	v_fmac_f32_e32 v22, v41, v57
	v_fmac_f32_e32 v19, v60, v64
	v_cndmask_b32_e32 v18, v23, v18, vcc
	s_waitcnt vmcnt(4)
	v_fmac_f32_e32 v22, v58, v66
	v_fmac_f32_e32 v19, v61, v65
	v_lshlrev_b32_e32 v18, 2, v18
	v_fmac_f32_e32 v22, v59, v67
	ds_bpermute_b32 v21, v18, v19
	v_fmac_f32_e32 v22, v60, v68
	v_fmac_f32_e32 v22, v61, v69
	ds_bpermute_b32 v25, v18, v22
	v_cvt_f16_f32_e32 v78, v41
	s_waitcnt lgkmcnt(1)
	v_add_f32_e32 v21, v19, v21
	v_xor_b32_e32 v19, 2, v23
	v_cmp_lt_i32_e32 vcc, v19, v24
	s_waitcnt lgkmcnt(0)
	v_add_f32_e32 v22, v22, v25
	v_cvt_f16_f32_e32 v26, v59
	v_cndmask_b32_e32 v19, v23, v19, vcc
	v_lshlrev_b32_e32 v19, 2, v19
	ds_bpermute_b32 v23, v19, v21
	ds_bpermute_b32 v24, v19, v22
	v_cvt_f16_f32_e32 v27, v60
	v_cvt_f16_f32_e32 v28, v61
	v_cmp_eq_u32_e32 vcc, 0, v1
	ds_write_b16 v76, v78 offset:54192
	ds_write_b16 v76, v26 offset:54736
	ds_write_b16 v76, v27 offset:55008
	ds_write_b16 v76, v28 offset:55280
	s_and_saveexec_b64 s[4:5], vcc
	s_cbranch_execz .LBB0_2
	v_lshlrev_b32_e32 v20, 2, v20
	v_or_b32_e32 v25, 0x10c00, v20
	s_waitcnt lgkmcnt(5)
	v_add_f32_e32 v21, v21, v23
	v_or_b32_e32 v20, 0x10e00, v20
	s_waitcnt lgkmcnt(4)
	v_add_f32_e32 v22, v22, v24
	ds_write_b32 v25, v21
	ds_write_b32 v20, v22

.LBB0_5:
	v_add_u32_e32 v2, 0xffffff00, v0
	v_ashrrev_i32_e32 v2, 2, v2
	v_lshlrev_b32_e32 v1, 7, v1
	v_mad_i32_i24 v3, v2, s3, v1
	ds_read_b128 v[4:7], v3
	v_or_b32_e32 v8, 0x10c00, v1
	v_or_b32_e32 v12, 0x10e00, v1
	ds_read_b128 v[8:11], v8
	ds_read_b128 v[12:15], v12
	ds_read_b128 v[20:23], v3 offset:16
	ds_read_b128 v[24:27], v3 offset:32
	ds_read_b128 v[28:31], v3 offset:48
	s_waitcnt lgkmcnt(4)
	v_fma_f32 v16, v4, v8, 0
	s_waitcnt lgkmcnt(3)
	v_fma_f32 v17, v4, v12, 0
	v_or_b32_e32 v4, 0x10c10, v1
	v_fmac_f32_e32 v16, v5, v9
	v_fmac_f32_e32 v17, v5, v13
	v_or_b32_e32 v5, 0x10e10, v1
	ds_read_b128 v[32:35], v4
	ds_read_b128 v[36:39], v5
	v_fmac_f32_e32 v16, v6, v10
	v_fmac_f32_e32 v17, v6, v14
	v_fmac_f32_e32 v16, v7, v11
	v_or_b32_e32 v4, 0x10c20, v1
	v_or_b32_e32 v8, 0x10e20, v1
	v_fmac_f32_e32 v17, v7, v15
	s_waitcnt lgkmcnt(1)
	v_fmac_f32_e32 v16, v20, v32
	ds_read_b128 v[4:7], v4
	ds_read_b128 v[8:11], v8
	v_fmac_f32_e32 v16, v21, v33
	s_waitcnt lgkmcnt(2)
	v_fmac_f32_e32 v17, v20, v36
	v_fmac_f32_e32 v16, v22, v34
	v_fmac_f32_e32 v17, v21, v37
	v_fmac_f32_e32 v16, v23, v35
	v_fmac_f32_e32 v17, v22, v38
	s_waitcnt lgkmcnt(1)
	v_fmac_f32_e32 v16, v24, v4
	v_or_b32_e32 v4, 0x10c30, v1
	v_fmac_f32_e32 v17, v23, v39
	v_fmac_f32_e32 v16, v25, v5
	v_or_b32_e32 v5, 0x10e30, v1
	ds_read_b128 v[12:15], v4
	ds_read_b128 v[20:23], v5
	s_waitcnt lgkmcnt(2)
	v_fmac_f32_e32 v17, v24, v8
	v_fmac_f32_e32 v17, v25, v9
	v_fmac_f32_e32 v16, v26, v6
	v_fmac_f32_e32 v17, v26, v10
	v_fmac_f32_e32 v16, v27, v7
	v_or_b32_e32 v8, 0x10c40, v1
	v_fmac_f32_e32 v17, v27, v11
	s_waitcnt lgkmcnt(1)
	v_fmac_f32_e32 v16, v28, v12
	ds_read_b128 v[4:7], v3 offset:64
	v_or_b32_e32 v12, 0x10e40, v1
	ds_read_b128 v[8:11], v8
	ds_read_b128 v[24:27], v12
	s_waitcnt lgkmcnt(3)
	v_fmac_f32_e32 v17, v28, v20
	v_fmac_f32_e32 v16, v29, v13
	v_fmac_f32_e32 v17, v29, v21
	v_fmac_f32_e32 v16, v30, v14
	v_fmac_f32_e32 v17, v30, v22
	v_fmac_f32_e32 v16, v31, v15
	v_fmac_f32_e32 v17, v31, v23
	s_waitcnt lgkmcnt(1)
	v_fmac_f32_e32 v16, v4, v8
	s_waitcnt lgkmcnt(0)
	v_fmac_f32_e32 v17, v4, v24
	v_or_b32_e32 v4, 0x10c50, v1
	ds_read_b128 v[12:15], v3 offset:80
	v_fmac_f32_e32 v16, v5, v9
	v_fmac_f32_e32 v17, v5, v25
	v_or_b32_e32 v5, 0x10e50, v1
	ds_read_b128 v[20:23], v4
	ds_read_b128 v[28:31], v5
	v_fmac_f32_e32 v16, v6, v10
	v_fmac_f32_e32 v17, v6, v26
	v_fmac_f32_e32 v16, v7, v11
	v_fmac_f32_e32 v17, v7, v27
	v_or_b32_e32 v8, 0x10c60, v1
	s_waitcnt lgkmcnt(1)
	v_fmac_f32_e32 v16, v12, v20
	s_waitcnt lgkmcnt(0)
	v_fmac_f32_e32 v17, v12, v28
	ds_read_b128 v[4:7], v3 offset:96
	v_or_b32_e32 v12, 0x10e60, v1
	ds_read_b128 v[8:11], v8
	ds_read_b128 v[24:27], v12
	v_fmac_f32_e32 v16, v13, v21
	v_fmac_f32_e32 v17, v13, v29
	v_fmac_f32_e32 v16, v14, v22
	v_fmac_f32_e32 v17, v14, v30
	v_fmac_f32_e32 v16, v15, v23
	v_fmac_f32_e32 v17, v15, v31
	ds_read_b128 v[12:15], v3 offset:112
	v_or_b32_e32 v3, 0x10c70, v1
	v_or_b32_e32 v1, 0x10e70, v1
	ds_read_b128 v[20:23], v3
	ds_read_b128 v[28:31], v1
	s_waitcnt lgkmcnt(4)
	v_fmac_f32_e32 v16, v4, v8
	s_waitcnt lgkmcnt(3)
	v_fmac_f32_e32 v17, v4, v24
	v_fmac_f32_e32 v16, v5, v9
	v_fmac_f32_e32 v17, v5, v25
	v_fmac_f32_e32 v16, v6, v10
	v_fmac_f32_e32 v17, v6, v26
	v_fmac_f32_e32 v16, v7, v11
	v_fmac_f32_e32 v17, v7, v27
	s_waitcnt lgkmcnt(1)
	v_fmac_f32_e32 v16, v12, v20
	s_waitcnt lgkmcnt(0)
	v_fmac_f32_e32 v17, v12, v28
	v_fmac_f32_e32 v16, v13, v21
	v_fmac_f32_e32 v17, v13, v29
	v_fmac_f32_e32 v16, v14, v22
	v_fmac_f32_e32 v17, v14, v30
	v_fmac_f32_e32 v16, v15, v23
	v_fmac_f32_e32 v17, v15, v31
	ds_bpermute_b32 v1, v18, v16
	ds_bpermute_b32 v3, v18, v17
	s_waitcnt lgkmcnt(1)
	v_add_f32_e32 v1, v16, v1
	s_waitcnt lgkmcnt(0)
	v_add_f32_e32 v3, v17, v3
	ds_bpermute_b32 v4, v19, v1
	ds_bpermute_b32 v5, v19, v3
	s_and_saveexec_b64 s[4:5], vcc
	s_cbranch_execz .LBB0_7
	s_mov_b64 s[8:9], s[40:41]
	s_mov_b64 s[10:11], s[42:43]
	v_add_u32_e32 v2, s2, v2
	s_waitcnt lgkmcnt(0)
	v_add_f32_e32 v6, v3, v5
	v_ashrrev_i32_e32 v3, 31, v2
	v_add_f32_e32 v1, v1, v4
	v_lshlrev_b64 v[2:3], 2, v[2:3]
	v_mul_f32_e32 v1, 0x3fb8aa3b, v1
	v_lshl_add_u64 v[4:5], s[8:9], 0, v[2:3]
	global_store_dword v[4:5], v1, off
	v_mul_f32_e32 v1, 0x3fb8aa3b, v6
	v_lshl_add_u64 v[2:3], s[10:11], 0, v[2:3]
	global_store_dword v[2:3], v1, off

.LBB0_8:
	s_lshr_b32 s3, s6, 2
	v_bfe_u32 v32, v0, 5, 1
	v_and_b32_e32 v33, 31, v0
	s_and_b32 s3, s3, 32
	v_or_b32_e32 v0, s3, v33
	s_waitcnt lgkmcnt(1)
	v_lshlrev_b32_e32 v4, 4, v32
	s_movk_i32 s4, 0x110
	v_mad_u32_u24 v36, v0, s4, v4
	ds_read_b128 v[0:3], v36 offset:33792
	s_bfe_u32 s7, s6, 0x10006
	s_waitcnt lgkmcnt(1)
	v_lshl_or_b32 v5, s7, 5, v33
	v_mad_u32_u24 v34, v5, s4, v4
	ds_read_b128 v[4:7], v34 offset:51200
	ds_read_b128 v[16:19], v36 offset:33824
	ds_read_b128 v[20:23], v34 offset:51232
	s_waitcnt lgkmcnt(2)
	v_mfma_f32_32x32x16_f16 v[0:15], v[0:3], v[4:7], 0
	v_lshlrev_b32_e32 v42, 3, v32
	v_lshlrev_b32_e32 v40, 4, v33
	s_mov_b64 s[0:1], s[38:39]
	s_ashr_i32 s4, s2, 11
	s_and_b32 s2, s2, 0x7c0
	s_ashr_i32 s5, s4, 31
	s_lshr_b32 s6, s6, 6
	s_waitcnt lgkmcnt(0)
	v_mfma_f32_32x32x16_f16 v[0:15], v[16:19], v[20:23], v[0:15]
	ds_read_b128 v[16:19], v36 offset:33856
	ds_read_b128 v[20:23], v34 offset:51264
	ds_read_b128 v[24:27], v34 offset:51296
	ds_read_b128 v[28:31], v36 offset:33888
	s_or_b32 s8, s3, s2
	s_lshl_b64 s[2:3], s[4:5], 18
	s_add_u32 s2, s0, s2
	s_addc_u32 s3, s1, s3
	s_lshr_b32 s4, s8, 3
	s_or_b32 s0, s4, s7
	s_waitcnt lgkmcnt(2)
	v_mfma_f32_32x32x16_f16 v[0:15], v[16:19], v[20:23], v[0:15]
	ds_read_b128 v[16:19], v36 offset:33920
	ds_read_b128 v[20:23], v34 offset:51328
	s_lshl_b32 s0, s0, 10
	s_add_u32 s0, s2, s0
	v_mov_b32_e32 v41, 0
	s_addc_u32 s1, s3, 0
	s_or_b32 s4, s4, s6
	s_waitcnt lgkmcnt(2)
	v_mfma_f32_32x32x16_f16 v[0:15], v[28:31], v[24:27], v[0:15]
	ds_read_b128 v[24:27], v34 offset:51360
	ds_read_b128 v[28:31], v36 offset:33952
	v_mov_b32_e32 v43, v41
	s_waitcnt lgkmcnt(2)
	v_mfma_f32_32x32x16_f16 v[0:15], v[16:19], v[20:23], v[0:15]
	ds_read_b128 v[16:19], v34 offset:51392
	ds_read_b128 v[20:23], v34 offset:51424
	ds_read_b128 v[32:35], v36 offset:33984
	ds_read_b128 v[36:39], v36 offset:34016
	s_waitcnt lgkmcnt(4)
	v_mfma_f32_32x32x16_f16 v[0:15], v[28:31], v[24:27], v[0:15]
	v_lshl_add_u64 v[24:25], s[0:1], 0, v[40:41]
	s_lshl_b32 s0, s4, 10
	s_bitset1_b32 s0, 11
	s_add_u32 s0, s2, s0
	s_addc_u32 s1, s3, 0
	s_waitcnt lgkmcnt(1)
	v_mfma_f32_32x32x16_f16 v[0:15], v[32:35], v[16:19], v[0:15]
	v_lshl_add_u64 v[16:17], v[24:25], 0, v[42:43]
	v_lshl_add_u64 v[18:19], s[0:1], 0, v[40:41]
	v_lshl_add_u64 v[18:19], v[18:19], 0, v[42:43]
	s_waitcnt lgkmcnt(0)
	v_mfma_f32_32x32x16_f16 v[0:15], v[36:39], v[20:23], v[0:15]
	s_nop 11
	v_cvt_pk_f16_f32 v3, v2, v3
	v_cvt_pk_f16_f32 v2, v0, v1
	v_cvt_pk_f16_f32 v1, v6, v7
	v_cvt_pk_f16_f32 v0, v4, v5
	v_cvt_pk_f16_f32 v5, v10, v11
	v_cvt_pk_f16_f32 v4, v8, v9
	v_cvt_pk_f16_f32 v7, v14, v15
	v_cvt_pk_f16_f32 v6, v12, v13
	global_store_dwordx2 v[16:17], v[2:3], off
	global_store_dwordx2 v[16:17], v[0:1], off offset:512
	global_store_dwordx2 v[18:19], v[4:5], off
	global_store_dwordx2 v[18:19], v[6:7], off offset:512
	s_endpgm

	.amdhsa_kernel _Z7gat_prePKfS0_S0_PDF16_PfS2_
		.amdhsa_group_segment_fixed_size 69632
		.amdhsa_private_segment_fixed_size 0
		.amdhsa_kernarg_size 48
		.amdhsa_user_sgpr_count 14
		.amdhsa_user_sgpr_dispatch_ptr 0
		.amdhsa_user_sgpr_queue_ptr 0
		.amdhsa_user_sgpr_kernarg_segment_ptr 1
		.amdhsa_user_sgpr_dispatch_id 0
		.amdhsa_user_sgpr_kernarg_preload_length 12
		.amdhsa_user_sgpr_kernarg_preload_offset 0
		.amdhsa_user_sgpr_private_segment_size 0
		.amdhsa_uses_dynamic_stack 0
		.amdhsa_enable_private_segment 0
		.amdhsa_system_sgpr_workgroup_id_x 1
		.amdhsa_system_sgpr_workgroup_id_y 0
		.amdhsa_system_sgpr_workgroup_id_z 0
		.amdhsa_system_sgpr_workgroup_info 0
		.amdhsa_system_vgpr_workitem_id 0
		.amdhsa_next_free_vgpr 97
		.amdhsa_next_free_sgpr 96
		.amdhsa_accum_offset 80
		.amdhsa_reserve_vcc 1
		.amdhsa_float_round_mode_32 0
		.amdhsa_float_round_mode_16_64 0
		.amdhsa_float_denorm_mode_32 3
		.amdhsa_float_denorm_mode_16_64 3
		.amdhsa_dx10_clamp 1
		.amdhsa_ieee_mode 1
		.amdhsa_fp16_overflow 0
		.amdhsa_tg_split 0
		.amdhsa_exception_fp_ieee_invalid_op 0
		.amdhsa_exception_fp_denorm_src 0
		.amdhsa_exception_fp_ieee_div_zero 0
		.amdhsa_exception_fp_ieee_overflow 0
		.amdhsa_exception_fp_ieee_underflow 0
		.amdhsa_exception_fp_ieee_inexact 0
		.amdhsa_exception_int_div_zero 0
	.end_amdhsa_kernel

_Z8gat_mainPKiPKDF16_PKfS4_Pf:
	s_mov_b32 s2, s12
	s_load_dwordx8 s[24:31], s[0:1], 0x0
	s_load_dwordx2 s[12:13], s[0:1], 0x20
	s_waitcnt lgkmcnt(0)
	s_branch .Lgm_body
	s_nop 0
	s_nop 0
	s_nop 0
	s_nop 0
	s_nop 0
	s_nop 0
	s_nop 0
	s_nop 0
	s_nop 0
	s_nop 0
	s_nop 0
	s_nop 0
	s_nop 0
	s_nop 0
	s_nop 0
	s_nop 0
	s_nop 0
	s_nop 0
	s_nop 0
	s_nop 0
	s_nop 0
	s_nop 0
	s_nop 0
	s_nop 0
	s_nop 0
	s_nop 0
	s_nop 0
	s_nop 0
	s_nop 0
	s_nop 0
	s_nop 0
	s_nop 0
	s_nop 0
	s_nop 0
	s_nop 0
	s_nop 0
	s_nop 0
	s_nop 0
	s_nop 0
	s_nop 0
	s_nop 0
	s_nop 0
	s_nop 0
	s_nop 0
	s_nop 0
	s_nop 0
	s_nop 0
	s_nop 0
	s_nop 0
	s_nop 0
	s_nop 0
	s_nop 0
	s_nop 0
	s_nop 0
	s_nop 0
	s_nop 0
	s_nop 0
.Lgm_preloaded:
	s_mov_b32 s81, s12
	s_mov_b64 s[24:25], s[2:3]
	s_mov_b64 s[26:27], s[4:5]
	s_mov_b64 s[28:29], s[6:7]
	s_mov_b64 s[30:31], s[8:9]
	s_mov_b64 s[12:13], s[10:11]
	s_mov_b32 s2, s81
.Lgm_body:
	v_and_b32_e32 v2, 63, v0
	v_readfirstlane_b32 s16, v0
	v_lshlrev_b32_e32 v1, 4, v2
	s_lshr_b32 s16, s16, 6
	s_and_b32 s17, s2, 7
	s_lshr_b32 s18, s2, 3
	s_lshr_b32 s19, s18, 3
	s_add_u32 s19, s19, s18
	s_and_b32 s19, s19, 7
	s_lshr_b32 s20, s16, 2
	s_and_b32 s21, s16, 3
	s_lshl_b32 s22, s16, 16
	s_lshl_b32 s23, s16, 12
	s_waitcnt lgkmcnt(0)
	s_lshl_b32 s3, s17, 24
	s_lshl_b32 s57, s18, 19
	s_add_u32 s3, s3, s57
	s_add_u32 s4, s24, s3
	s_addc_u32 s5, s25, 0
	s_and_b32 s5, s5, 0xffff
	s_mov_b32 s6, 0x80000
	s_mov_b32 s7, 0x20000
	s_lshl_b32 s3, s17, 18
	s_add_u32 s8, s26, s3
	s_addc_u32 s9, s27, 0
	s_and_b32 s9, s9, 0xffff
	s_mov_b32 s10, 0x40000
	s_mov_b32 s11, 0x20000
	s_lshl_b32 s3, s17, 11
	s_lshl_b32 s57, s18, 6
	s_add_u32 s3, s3, s57
	s_lshl_b32 s57, s16, 3
	s_add_u32 s3, s3, s57
	s_lshl_b32 s3, s3, 2
	s_add_u32 s28, s28, s3
	s_addc_u32 s29, s29, 0
	v_and_b32_e32 v36, 7, v0
	v_lshlrev_b32_e32 v36, 2, v36
	global_load_dword v37, v36, s[28:29]
	s_lshl_b32 s3, s17, 13
	s_add_u32 s30, s30, s3
	s_addc_u32 s31, s31, 0
	v_lshlrev_b32_e32 v38, 4, v0
	global_load_dwordx4 v[24:27], v38, s[30:31]
	s_add_u32 s3, s19, 0
	s_and_b32 s3, s3, 7
	s_lshl_b32 s57, s3, 10
	s_add_u32 s48, s57, s22
	s_add_u32 s49, s48, 0x2000
	s_add_u32 s50, s48, 0x4000
	s_add_u32 s51, s48, 0x6000
	s_add_u32 s52, s48, 0x8000
	s_add_u32 s53, s48, 0xa000
	s_add_u32 s54, s48, 0xc000
	s_add_u32 s55, s48, 0xe000
	s_lshl_b32 s56, s3, 15
	s_add_u32 s56, s56, s23
	buffer_load_dwordx4 v[88:91], v1, s[4:7], s48 offen nt
	buffer_load_dwordx4 v[92:95], v1, s[4:7], s49 offen nt
	buffer_load_dwordx4 v[96:99], v1, s[4:7], s50 offen nt
	buffer_load_dwordx4 v[100:103], v1, s[4:7], s51 offen nt
	buffer_load_dwordx4 v[104:107], v1, s[4:7], s52 offen nt
	buffer_load_dwordx4 v[108:111], v1, s[4:7], s53 offen nt
	buffer_load_dwordx4 v[112:115], v1, s[4:7], s54 offen nt
	buffer_load_dwordx4 v[116:119], v1, s[4:7], s55 offen nt
	buffer_load_dwordx4 v[152:155], v1, s[8:11], s56 offen
	buffer_load_dwordx4 v[156:159], v1, s[8:11], s56 offen offset:1024
	buffer_load_dwordx4 v[160:163], v1, s[8:11], s56 offen offset:2048
	buffer_load_dwordx4 v[164:167], v1, s[8:11], s56 offen offset:3072
	s_mul_i32 s3, s16, 0x1080
	v_lshlrev_b32_e32 v3, 3, v2
	v_add_u32_e32 v3, s3, v3
	v_add_u32_e32 v4, 0x840, v3
	v_add_u32_e32 v5, 0x8400, v3
	v_add_u32_e32 v6, 0x8400, v4
	v_and_b32_e32 v36, 31, v2
	v_mul_u32_u24_e32 v36, 0x210, v36
	v_lshrrev_b32_e32 v38, 5, v2
	v_lshlrev_b32_e32 v38, 4, v38
	v_add_u32_e32 v7, v36, v38
	s_mul_i32 s3, s20, 0x4200
	s_lshl_b32 s57, s21, 7
	s_add_u32 s3, s3, s57
	v_add_u32_e32 v7, s3, v7
	s_lshl_b32 s3, s21, 13
	s_add_u32 s3, s3, 0x14800
	v_add_u32_e32 v8, s3, v1
	s_add_u32 s3, s23, 0x14800
	v_add_u32_e32 v9, s3, v1
	v_add_u32_e32 v10, 0x10800, v1
	v_mov_b32_e32 v12, 0x3c003c00
	v_mov_b32_e32 v13, 0x3c003c00
	v_mov_b32_e32 v14, 0x3c003c00
	v_mov_b32_e32 v15, 0x3c003c00
	v_mov_b32_e32 v40, 0
	v_mov_b32_e32 v41, 0
	v_mov_b32_e32 v42, 0
	v_mov_b32_e32 v43, 0
	v_mov_b32_e32 v44, 0
	v_mov_b32_e32 v45, 0
	v_mov_b32_e32 v46, 0
	v_mov_b32_e32 v47, 0
	v_mov_b32_e32 v48, 0
	v_mov_b32_e32 v49, 0
	v_mov_b32_e32 v50, 0
	v_mov_b32_e32 v51, 0
	v_mov_b32_e32 v52, 0
	v_mov_b32_e32 v53, 0
	v_mov_b32_e32 v54, 0
	v_mov_b32_e32 v55, 0
	v_mov_b32_e32 v56, 0
	v_mov_b32_e32 v57, 0
	v_mov_b32_e32 v58, 0
	v_mov_b32_e32 v59, 0
	v_mov_b32_e32 v60, 0
	v_mov_b32_e32 v61, 0
	v_mov_b32_e32 v62, 0
	v_mov_b32_e32 v63, 0
	v_mov_b32_e32 v64, 0
	v_mov_b32_e32 v65, 0
	v_mov_b32_e32 v66, 0
	v_mov_b32_e32 v67, 0
	v_mov_b32_e32 v68, 0
	v_mov_b32_e32 v69, 0
	v_mov_b32_e32 v70, 0
	v_mov_b32_e32 v71, 0
	v_mov_b32_e32 v72, 0
	v_mov_b32_e32 v73, 0
	v_mov_b32_e32 v74, 0
	v_mov_b32_e32 v75, 0
	v_mov_b32_e32 v76, 0
	v_mov_b32_e32 v77, 0
	v_mov_b32_e32 v78, 0
	v_mov_b32_e32 v79, 0
	v_mov_b32_e32 v80, 0
	v_mov_b32_e32 v81, 0
	v_mov_b32_e32 v82, 0
	v_mov_b32_e32 v83, 0
	v_mov_b32_e32 v84, 0
	v_mov_b32_e32 v85, 0
	v_mov_b32_e32 v86, 0
	v_mov_b32_e32 v87, 0
	s_lshl_b32 s3, s17, 11
	s_lshl_b32 s57, s18, 6
	s_add_u32 s3, s3, s57
	s_lshl_b32 s57, s20, 5
	s_add_u32 s3, s3, s57
	s_lshl_b32 s57, s21, 3
	s_add_u32 s3, s3, s57
	s_lshl_b32 s3, s3, 8
	s_add_u32 s12, s12, s3
	s_addc_u32 s13, s13, 0
	s_waitcnt vmcnt(12)
	v_max_f32_e32 v28, v24, v25
	v_max3_f32 v28, v28, v26, v27
	v_lshlrev_b32_e32 v29, 2, v2
	v_xor_b32_e32 v30, 4, v29
	ds_bpermute_b32 v31, v30, v28
	s_waitcnt lgkmcnt(0)
	v_max_f32_e32 v28, v28, v31
	v_xor_b32_e32 v30, 8, v29
	ds_bpermute_b32 v31, v30, v28
	s_waitcnt lgkmcnt(0)
	v_max_f32_e32 v28, v28, v31
	v_xor_b32_e32 v30, 16, v29
	ds_bpermute_b32 v31, v30, v28
	s_waitcnt lgkmcnt(0)
	v_max_f32_e32 v28, v28, v31
	v_xor_b32_e32 v30, 32, v29
	ds_bpermute_b32 v31, v30, v28
	s_waitcnt lgkmcnt(0)
	v_max_f32_e32 v28, v28, v31
	v_xor_b32_e32 v30, 64, v29
	ds_bpermute_b32 v31, v30, v28
	s_waitcnt lgkmcnt(0)
	v_max_f32_e32 v28, v28, v31
	v_xor_b32_e32 v30, 128, v29
	ds_bpermute_b32 v31, v30, v28
	s_waitcnt lgkmcnt(0)
	v_max_f32_e32 v28, v28, v31
	s_lshl_b32 s3, s16, 2
	s_add_u32 s3, s3, 0x24800
	v_mov_b32_e32 v30, s3
	ds_write_b32 v30, v28
	s_waitcnt lgkmcnt(0)
	s_barrier
	v_mov_b32_e32 v30, 0x24800
	ds_read_b128 v[32:35], v30
	ds_read_b128 v[16:19], v30 offset:16
	s_waitcnt lgkmcnt(0)
	v_max3_f32 v28, v32, v33, v34
	v_max3_f32 v28, v28, v35, v16
	v_max3_f32 v28, v28, v17, v18
	v_max_f32_e32 v28, v28, v19
	v_sub_f32_e32 v16, v24, v28
	v_sub_f32_e32 v17, v25, v28
	v_sub_f32_e32 v18, v26, v28
	v_sub_f32_e32 v19, v27, v28
	v_mul_f32_e32 v20, 0x3e4ccccd, v16
	v_mul_f32_e32 v21, 0x3e4ccccd, v17
	v_mul_f32_e32 v22, 0x3e4ccccd, v18
	v_mul_f32_e32 v23, 0x3e4ccccd, v19
	v_exp_f32_e32 v16, v16
	v_exp_f32_e32 v17, v17
	v_exp_f32_e32 v18, v18
	v_exp_f32_e32 v19, v19
	v_exp_f32_e32 v20, v20
	v_exp_f32_e32 v21, v21
	v_exp_f32_e32 v22, v22
	v_exp_f32_e32 v23, v23
	v_lshlrev_b32_e32 v30, 4, v0
	v_add_u32_e32 v30, 0x10800, v30
	ds_write_b128 v30, v[16:19]
	ds_write_b128 v30, v[20:23] offset:8192
	v_add_f32_e32 v36, v37, v28
	v_mul_f32_e32 v38, 0x3e4ccccd, v36
	v_max_f32_e32 v39, v36, v38
	v_sub_f32_e32 v36, v36, v39
	v_sub_f32_e32 v38, v38, v39
	v_add_f32_e32 v36, 0x41600000, v36
	v_add_f32_e32 v38, 0x41600000, v38
	v_exp_f32_e32 v36, v36
	v_exp_f32_e32 v38, v38
	s_nop 1
	v_readlane_b32 s32, v36, 0
	v_readlane_b32 s33, v36, 1
	v_readlane_b32 s34, v36, 2
	v_readlane_b32 s35, v36, 3
	v_readlane_b32 s36, v36, 4
	v_readlane_b32 s37, v36, 5
	v_readlane_b32 s38, v36, 6
	v_readlane_b32 s39, v36, 7
	v_readlane_b32 s40, v38, 0
	v_readlane_b32 s41, v38, 1
	v_readlane_b32 s42, v38, 2
	v_readlane_b32 s43, v38, 3
	v_readlane_b32 s44, v38, 4
	v_readlane_b32 s45, v38, 5
	v_readlane_b32 s46, v38, 6
	v_readlane_b32 s47, v38, 7
	s_waitcnt lgkmcnt(0)
	s_barrier
	s_lshl_b32 s3, s19, 10
	v_add_u32_e32 v11, s3, v10
	ds_read_b128 v[16:19], v11
	ds_read_b128 v[20:23], v11 offset:8192
	s_waitcnt lgkmcnt(0)
	s_add_u32 s3, s19, 1
	s_and_b32 s3, s3, 7
	s_lshl_b32 s57, s3, 10
	s_add_u32 s48, s57, s22
	s_add_u32 s49, s48, 0x2000
	s_add_u32 s50, s48, 0x4000
	s_add_u32 s51, s48, 0x6000
	s_add_u32 s52, s48, 0x8000
	s_add_u32 s53, s48, 0xa000
	s_add_u32 s54, s48, 0xc000
	s_add_u32 s55, s48, 0xe000
	s_lshl_b32 s56, s3, 15
	s_add_u32 s56, s56, s23
	buffer_load_dwordx4 v[120:123], v1, s[4:7], s48 offen nt
	buffer_load_dwordx4 v[124:127], v1, s[4:7], s49 offen nt
	buffer_load_dwordx4 v[128:131], v1, s[4:7], s50 offen nt
	buffer_load_dwordx4 v[132:135], v1, s[4:7], s51 offen nt
	buffer_load_dwordx4 v[136:139], v1, s[4:7], s52 offen nt
	buffer_load_dwordx4 v[140:143], v1, s[4:7], s53 offen nt
	buffer_load_dwordx4 v[144:147], v1, s[4:7], s54 offen nt
	buffer_load_dwordx4 v[148:151], v1, s[4:7], s55 offen nt
	buffer_load_dwordx4 v[168:171], v1, s[8:11], s56 offen
	buffer_load_dwordx4 v[172:175], v1, s[8:11], s56 offen offset:1024
	buffer_load_dwordx4 v[176:179], v1, s[8:11], s56 offen offset:2048
	buffer_load_dwordx4 v[180:183], v1, s[8:11], s56 offen offset:3072
	s_waitcnt vmcnt(12)
	v_pk_mul_f32 v[24:25], v[16:17], s[32:33] op_sel_hi:[1,0]
	v_pk_mul_f32 v[26:27], v[18:19], s[32:33] op_sel_hi:[1,0]
	v_pk_mul_f32 v[28:29], v[20:21], s[40:41] op_sel_hi:[1,0]
	v_pk_mul_f32 v[30:31], v[22:23], s[40:41] op_sel_hi:[1,0]
	v_cmp_lt_i32_e64 s[60:61], 0, v88
	v_cmp_lt_i32_e64 s[62:63], 0, v89
	v_cmp_lt_i32_e64 s[64:65], 0, v90
	v_cmp_lt_i32_e64 s[66:67], 0, v91
	v_max_f32_e32 v24, v24, v28
	v_max_f32_e32 v25, v25, v29
	v_max_f32_e32 v26, v26, v30
	v_max_f32_e32 v27, v27, v31
	v_cndmask_b32_e64 v24, 0, v24, s[60:61]
	v_cndmask_b32_e64 v25, 0, v25, s[62:63]
	v_cndmask_b32_e64 v26, 0, v26, s[64:65]
	v_cndmask_b32_e64 v27, 0, v27, s[66:67]
	v_cvt_pkrtz_f16_f32 v32, v24, v25
	v_cvt_pkrtz_f16_f32 v33, v26, v27
	v_pk_mul_f32 v[24:25], v[16:17], s[32:33] op_sel:[0,1] op_sel_hi:[1,1]
	v_pk_mul_f32 v[26:27], v[18:19], s[32:33] op_sel:[0,1] op_sel_hi:[1,1]
	v_pk_mul_f32 v[28:29], v[20:21], s[40:41] op_sel:[0,1] op_sel_hi:[1,1]
	v_pk_mul_f32 v[30:31], v[22:23], s[40:41] op_sel:[0,1] op_sel_hi:[1,1]
	v_cmp_lt_i32_e64 s[60:61], 0, v92
	v_cmp_lt_i32_e64 s[62:63], 0, v93
	v_cmp_lt_i32_e64 s[64:65], 0, v94
	v_cmp_lt_i32_e64 s[66:67], 0, v95
	v_max_f32_e32 v24, v24, v28
	v_max_f32_e32 v25, v25, v29
	v_max_f32_e32 v26, v26, v30
	v_max_f32_e32 v27, v27, v31
	v_cndmask_b32_e64 v24, 0, v24, s[60:61]
	v_cndmask_b32_e64 v25, 0, v25, s[62:63]
	v_cndmask_b32_e64 v26, 0, v26, s[64:65]
	v_cndmask_b32_e64 v27, 0, v27, s[66:67]
	v_cvt_pkrtz_f16_f32 v34, v24, v25
	v_cvt_pkrtz_f16_f32 v35, v26, v27
	ds_write2_b64 v3, v[32:33], v[34:35] offset0:0 offset1:66
	v_pk_mul_f32 v[24:25], v[16:17], s[34:35] op_sel_hi:[1,0]
	v_pk_mul_f32 v[26:27], v[18:19], s[34:35] op_sel_hi:[1,0]
	v_pk_mul_f32 v[28:29], v[20:21], s[42:43] op_sel_hi:[1,0]
	v_pk_mul_f32 v[30:31], v[22:23], s[42:43] op_sel_hi:[1,0]
	v_cmp_lt_i32_e64 s[60:61], 0, v96
	v_cmp_lt_i32_e64 s[62:63], 0, v97
	v_cmp_lt_i32_e64 s[64:65], 0, v98
	v_cmp_lt_i32_e64 s[66:67], 0, v99
	v_max_f32_e32 v24, v24, v28
	v_max_f32_e32 v25, v25, v29
	v_max_f32_e32 v26, v26, v30
	v_max_f32_e32 v27, v27, v31
	v_cndmask_b32_e64 v24, 0, v24, s[60:61]
	v_cndmask_b32_e64 v25, 0, v25, s[62:63]
	v_cndmask_b32_e64 v26, 0, v26, s[64:65]
	v_cndmask_b32_e64 v27, 0, v27, s[66:67]
	v_cvt_pkrtz_f16_f32 v32, v24, v25
	v_cvt_pkrtz_f16_f32 v33, v26, v27
	v_pk_mul_f32 v[24:25], v[16:17], s[34:35] op_sel:[0,1] op_sel_hi:[1,1]
	v_pk_mul_f32 v[26:27], v[18:19], s[34:35] op_sel:[0,1] op_sel_hi:[1,1]
	v_pk_mul_f32 v[28:29], v[20:21], s[42:43] op_sel:[0,1] op_sel_hi:[1,1]
	v_pk_mul_f32 v[30:31], v[22:23], s[42:43] op_sel:[0,1] op_sel_hi:[1,1]
	v_cmp_lt_i32_e64 s[60:61], 0, v100
	v_cmp_lt_i32_e64 s[62:63], 0, v101
	v_cmp_lt_i32_e64 s[64:65], 0, v102
	v_cmp_lt_i32_e64 s[66:67], 0, v103
	v_max_f32_e32 v24, v24, v28
	v_max_f32_e32 v25, v25, v29
	v_max_f32_e32 v26, v26, v30
	v_max_f32_e32 v27, v27, v31
	v_cndmask_b32_e64 v24, 0, v24, s[60:61]
	v_cndmask_b32_e64 v25, 0, v25, s[62:63]
	v_cndmask_b32_e64 v26, 0, v26, s[64:65]
	v_cndmask_b32_e64 v27, 0, v27, s[66:67]
	v_cvt_pkrtz_f16_f32 v34, v24, v25
	v_cvt_pkrtz_f16_f32 v35, v26, v27
	ds_write2_b64 v3, v[32:33], v[34:35] offset0:132 offset1:198
	v_pk_mul_f32 v[24:25], v[16:17], s[36:37] op_sel_hi:[1,0]
	v_pk_mul_f32 v[26:27], v[18:19], s[36:37] op_sel_hi:[1,0]
	v_pk_mul_f32 v[28:29], v[20:21], s[44:45] op_sel_hi:[1,0]
	v_pk_mul_f32 v[30:31], v[22:23], s[44:45] op_sel_hi:[1,0]
	v_cmp_lt_i32_e64 s[60:61], 0, v104
	v_cmp_lt_i32_e64 s[62:63], 0, v105
	v_cmp_lt_i32_e64 s[64:65], 0, v106
	v_cmp_lt_i32_e64 s[66:67], 0, v107
	v_max_f32_e32 v24, v24, v28
	v_max_f32_e32 v25, v25, v29
	v_max_f32_e32 v26, v26, v30
	v_max_f32_e32 v27, v27, v31
	v_cndmask_b32_e64 v24, 0, v24, s[60:61]
	v_cndmask_b32_e64 v25, 0, v25, s[62:63]
	v_cndmask_b32_e64 v26, 0, v26, s[64:65]
	v_cndmask_b32_e64 v27, 0, v27, s[66:67]
	v_cvt_pkrtz_f16_f32 v32, v24, v25
	v_cvt_pkrtz_f16_f32 v33, v26, v27
	v_pk_mul_f32 v[24:25], v[16:17], s[36:37] op_sel:[0,1] op_sel_hi:[1,1]
	v_pk_mul_f32 v[26:27], v[18:19], s[36:37] op_sel:[0,1] op_sel_hi:[1,1]
	v_pk_mul_f32 v[28:29], v[20:21], s[44:45] op_sel:[0,1] op_sel_hi:[1,1]
	v_pk_mul_f32 v[30:31], v[22:23], s[44:45] op_sel:[0,1] op_sel_hi:[1,1]
	v_cmp_lt_i32_e64 s[60:61], 0, v108
	v_cmp_lt_i32_e64 s[62:63], 0, v109
	v_cmp_lt_i32_e64 s[64:65], 0, v110
	v_cmp_lt_i32_e64 s[66:67], 0, v111
	v_max_f32_e32 v24, v24, v28
	v_max_f32_e32 v25, v25, v29
	v_max_f32_e32 v26, v26, v30
	v_max_f32_e32 v27, v27, v31
	v_cndmask_b32_e64 v24, 0, v24, s[60:61]
	v_cndmask_b32_e64 v25, 0, v25, s[62:63]
	v_cndmask_b32_e64 v26, 0, v26, s[64:65]
	v_cndmask_b32_e64 v27, 0, v27, s[66:67]
	v_cvt_pkrtz_f16_f32 v34, v24, v25
	v_cvt_pkrtz_f16_f32 v35, v26, v27
	ds_write2_b64 v4, v[32:33], v[34:35] offset0:0 offset1:66
	v_pk_mul_f32 v[24:25], v[16:17], s[38:39] op_sel_hi:[1,0]
	v_pk_mul_f32 v[26:27], v[18:19], s[38:39] op_sel_hi:[1,0]
	v_pk_mul_f32 v[28:29], v[20:21], s[46:47] op_sel_hi:[1,0]
	v_pk_mul_f32 v[30:31], v[22:23], s[46:47] op_sel_hi:[1,0]
	v_cmp_lt_i32_e64 s[60:61], 0, v112
	v_cmp_lt_i32_e64 s[62:63], 0, v113
	v_cmp_lt_i32_e64 s[64:65], 0, v114
	v_cmp_lt_i32_e64 s[66:67], 0, v115
	v_max_f32_e32 v24, v24, v28
	v_max_f32_e32 v25, v25, v29
	v_max_f32_e32 v26, v26, v30
	v_max_f32_e32 v27, v27, v31
	v_cndmask_b32_e64 v24, 0, v24, s[60:61]
	v_cndmask_b32_e64 v25, 0, v25, s[62:63]
	v_cndmask_b32_e64 v26, 0, v26, s[64:65]
	v_cndmask_b32_e64 v27, 0, v27, s[66:67]
	v_cvt_pkrtz_f16_f32 v32, v24, v25
	v_cvt_pkrtz_f16_f32 v33, v26, v27
	v_pk_mul_f32 v[24:25], v[16:17], s[38:39] op_sel:[0,1] op_sel_hi:[1,1]
	v_pk_mul_f32 v[26:27], v[18:19], s[38:39] op_sel:[0,1] op_sel_hi:[1,1]
	v_pk_mul_f32 v[28:29], v[20:21], s[46:47] op_sel:[0,1] op_sel_hi:[1,1]
	v_pk_mul_f32 v[30:31], v[22:23], s[46:47] op_sel:[0,1] op_sel_hi:[1,1]
	v_cmp_lt_i32_e64 s[60:61], 0, v116
	v_cmp_lt_i32_e64 s[62:63], 0, v117
	v_cmp_lt_i32_e64 s[64:65], 0, v118
	v_cmp_lt_i32_e64 s[66:67], 0, v119
	v_max_f32_e32 v24, v24, v28
	v_max_f32_e32 v25, v25, v29
	v_max_f32_e32 v26, v26, v30
	v_max_f32_e32 v27, v27, v31
	v_cndmask_b32_e64 v24, 0, v24, s[60:61]
	v_cndmask_b32_e64 v25, 0, v25, s[62:63]
	v_cndmask_b32_e64 v26, 0, v26, s[64:65]
	v_cndmask_b32_e64 v27, 0, v27, s[66:67]
	v_cvt_pkrtz_f16_f32 v34, v24, v25
	v_cvt_pkrtz_f16_f32 v35, v26, v27
	ds_write2_b64 v4, v[32:33], v[34:35] offset0:132 offset1:198
	ds_write_b128 v9, v[152:155] offset:0
	ds_write_b128 v9, v[156:159] offset:1024
	ds_write_b128 v9, v[160:163] offset:2048
	ds_write_b128 v9, v[164:167] offset:3072
	s_add_u32 s3, s19, 1
	s_and_b32 s3, s3, 7
	s_lshl_b32 s3, s3, 10
	v_add_u32_e32 v11, s3, v10
	ds_read_b128 v[16:19], v11
	ds_read_b128 v[20:23], v11 offset:8192
	s_waitcnt lgkmcnt(0)
	s_barrier
	ds_read_b128 v[184:187], v7 offset:0
	ds_read_b128 v[200:203], v8 offset:0
	ds_read_b128 v[204:207], v8 offset:1024
	ds_read_b128 v[188:191], v7 offset:32
	ds_read_b128 v[208:211], v8 offset:2048
	ds_read_b128 v[212:215], v8 offset:3072
	ds_read_b128 v[192:195], v7 offset:64
	ds_read_b128 v[216:219], v8 offset:4096
	ds_read_b128 v[220:223], v8 offset:5120
	ds_read_b128 v[196:199], v7 offset:96
	ds_read_b128 v[224:227], v8 offset:6144
	ds_read_b128 v[228:231], v8 offset:7168
	s_add_u32 s3, s19, 2
	s_and_b32 s3, s3, 7
	s_lshl_b32 s57, s3, 10
	s_add_u32 s48, s57, s22
	s_add_u32 s49, s48, 0x2000
	s_add_u32 s50, s48, 0x4000
	s_add_u32 s51, s48, 0x6000
	s_add_u32 s52, s48, 0x8000
	s_add_u32 s53, s48, 0xa000
	s_add_u32 s54, s48, 0xc000
	s_add_u32 s55, s48, 0xe000
	s_lshl_b32 s56, s3, 15
	s_add_u32 s56, s56, s23
	buffer_load_dwordx4 v[88:91], v1, s[4:7], s48 offen nt
	buffer_load_dwordx4 v[92:95], v1, s[4:7], s49 offen nt
	buffer_load_dwordx4 v[96:99], v1, s[4:7], s50 offen nt
	buffer_load_dwordx4 v[100:103], v1, s[4:7], s51 offen nt
	buffer_load_dwordx4 v[104:107], v1, s[4:7], s52 offen nt
	buffer_load_dwordx4 v[108:111], v1, s[4:7], s53 offen nt
	buffer_load_dwordx4 v[112:115], v1, s[4:7], s54 offen nt
	buffer_load_dwordx4 v[116:119], v1, s[4:7], s55 offen nt
	buffer_load_dwordx4 v[152:155], v1, s[8:11], s56 offen
	buffer_load_dwordx4 v[156:159], v1, s[8:11], s56 offen offset:1024
	buffer_load_dwordx4 v[160:163], v1, s[8:11], s56 offen offset:2048
	buffer_load_dwordx4 v[164:167], v1, s[8:11], s56 offen offset:3072
	s_waitcnt vmcnt(12)
	v_pk_mul_f32 v[24:25], v[16:17], s[32:33] op_sel_hi:[1,0]
	v_pk_mul_f32 v[26:27], v[18:19], s[32:33] op_sel_hi:[1,0]
	v_pk_mul_f32 v[28:29], v[20:21], s[40:41] op_sel_hi:[1,0]
	v_pk_mul_f32 v[30:31], v[22:23], s[40:41] op_sel_hi:[1,0]
	v_cmp_lt_i32_e64 s[60:61], 0, v120
	v_cmp_lt_i32_e64 s[62:63], 0, v121
	v_cmp_lt_i32_e64 s[64:65], 0, v122
	v_cmp_lt_i32_e64 s[66:67], 0, v123
	v_max_f32_e32 v24, v24, v28
	v_max_f32_e32 v25, v25, v29
	v_max_f32_e32 v26, v26, v30
	v_max_f32_e32 v27, v27, v31
	v_cndmask_b32_e64 v24, 0, v24, s[60:61]
	v_cndmask_b32_e64 v25, 0, v25, s[62:63]
	v_cndmask_b32_e64 v26, 0, v26, s[64:65]
	v_cndmask_b32_e64 v27, 0, v27, s[66:67]
	v_cvt_pkrtz_f16_f32 v32, v24, v25
	v_cvt_pkrtz_f16_f32 v33, v26, v27
	s_waitcnt lgkmcnt(0)
	v_pk_mul_f32 v[24:25], v[16:17], s[32:33] op_sel:[0,1] op_sel_hi:[1,1]
	v_pk_mul_f32 v[26:27], v[18:19], s[32:33] op_sel:[0,1] op_sel_hi:[1,1]
	v_pk_mul_f32 v[28:29], v[20:21], s[40:41] op_sel:[0,1] op_sel_hi:[1,1]
	v_pk_mul_f32 v[30:31], v[22:23], s[40:41] op_sel:[0,1] op_sel_hi:[1,1]
	v_mfma_f32_32x32x16_f16 v[40:55], v[184:187], v[200:203], v[40:55]
	v_cmp_lt_i32_e64 s[60:61], 0, v124
	v_cmp_lt_i32_e64 s[62:63], 0, v125
	v_cmp_lt_i32_e64 s[64:65], 0, v126
	v_cmp_lt_i32_e64 s[66:67], 0, v127
	v_max_f32_e32 v24, v24, v28
	v_max_f32_e32 v25, v25, v29
	v_max_f32_e32 v26, v26, v30
	v_max_f32_e32 v27, v27, v31
	v_cndmask_b32_e64 v24, 0, v24, s[60:61]
	v_cndmask_b32_e64 v25, 0, v25, s[62:63]
	v_cndmask_b32_e64 v26, 0, v26, s[64:65]
	v_cndmask_b32_e64 v27, 0, v27, s[66:67]
	v_mfma_f32_32x32x16_f16 v[56:71], v[184:187], v[204:207], v[56:71]
	v_cvt_pkrtz_f16_f32 v34, v24, v25
	v_cvt_pkrtz_f16_f32 v35, v26, v27
	ds_write2_b64 v5, v[32:33], v[34:35] offset0:0 offset1:66
	v_pk_mul_f32 v[24:25], v[16:17], s[34:35] op_sel_hi:[1,0]
	v_pk_mul_f32 v[26:27], v[18:19], s[34:35] op_sel_hi:[1,0]
	v_pk_mul_f32 v[28:29], v[20:21], s[42:43] op_sel_hi:[1,0]
	v_pk_mul_f32 v[30:31], v[22:23], s[42:43] op_sel_hi:[1,0]
	v_mfma_f32_32x32x16_f16 v[72:87], v[184:187], v[12:15], v[72:87]
	v_cmp_lt_i32_e64 s[60:61], 0, v128
	v_cmp_lt_i32_e64 s[62:63], 0, v129
	v_cmp_lt_i32_e64 s[64:65], 0, v130
	v_cmp_lt_i32_e64 s[66:67], 0, v131
	v_max_f32_e32 v24, v24, v28
	v_max_f32_e32 v25, v25, v29
	v_max_f32_e32 v26, v26, v30
	v_max_f32_e32 v27, v27, v31
	v_cndmask_b32_e64 v24, 0, v24, s[60:61]
	v_cndmask_b32_e64 v25, 0, v25, s[62:63]
	v_cndmask_b32_e64 v26, 0, v26, s[64:65]
	v_cndmask_b32_e64 v27, 0, v27, s[66:67]
	v_mfma_f32_32x32x16_f16 v[40:55], v[188:191], v[208:211], v[40:55]
	v_cvt_pkrtz_f16_f32 v32, v24, v25
	v_cvt_pkrtz_f16_f32 v33, v26, v27
	v_pk_mul_f32 v[24:25], v[16:17], s[34:35] op_sel:[0,1] op_sel_hi:[1,1]
	v_pk_mul_f32 v[26:27], v[18:19], s[34:35] op_sel:[0,1] op_sel_hi:[1,1]
	v_pk_mul_f32 v[28:29], v[20:21], s[42:43] op_sel:[0,1] op_sel_hi:[1,1]
	v_pk_mul_f32 v[30:31], v[22:23], s[42:43] op_sel:[0,1] op_sel_hi:[1,1]
	v_mfma_f32_32x32x16_f16 v[56:71], v[188:191], v[212:215], v[56:71]
	v_cmp_lt_i32_e64 s[60:61], 0, v132
	v_cmp_lt_i32_e64 s[62:63], 0, v133
	v_cmp_lt_i32_e64 s[64:65], 0, v134
	v_cmp_lt_i32_e64 s[66:67], 0, v135
	v_max_f32_e32 v24, v24, v28
	v_max_f32_e32 v25, v25, v29
	v_max_f32_e32 v26, v26, v30
	v_max_f32_e32 v27, v27, v31
	v_cndmask_b32_e64 v24, 0, v24, s[60:61]
	v_cndmask_b32_e64 v25, 0, v25, s[62:63]
	v_cndmask_b32_e64 v26, 0, v26, s[64:65]
	v_cndmask_b32_e64 v27, 0, v27, s[66:67]
	v_mfma_f32_32x32x16_f16 v[72:87], v[188:191], v[12:15], v[72:87]
	v_cvt_pkrtz_f16_f32 v34, v24, v25
	v_cvt_pkrtz_f16_f32 v35, v26, v27
	ds_write2_b64 v5, v[32:33], v[34:35] offset0:132 offset1:198
	v_pk_mul_f32 v[24:25], v[16:17], s[36:37] op_sel_hi:[1,0]
	v_pk_mul_f32 v[26:27], v[18:19], s[36:37] op_sel_hi:[1,0]
	v_pk_mul_f32 v[28:29], v[20:21], s[44:45] op_sel_hi:[1,0]
	v_pk_mul_f32 v[30:31], v[22:23], s[44:45] op_sel_hi:[1,0]
	v_mfma_f32_32x32x16_f16 v[40:55], v[192:195], v[216:219], v[40:55]
	v_cmp_lt_i32_e64 s[60:61], 0, v136
	v_cmp_lt_i32_e64 s[62:63], 0, v137
	v_cmp_lt_i32_e64 s[64:65], 0, v138
	v_cmp_lt_i32_e64 s[66:67], 0, v139
	v_max_f32_e32 v24, v24, v28
	v_max_f32_e32 v25, v25, v29
	v_max_f32_e32 v26, v26, v30
	v_max_f32_e32 v27, v27, v31
	v_cndmask_b32_e64 v24, 0, v24, s[60:61]
	v_cndmask_b32_e64 v25, 0, v25, s[62:63]
	v_cndmask_b32_e64 v26, 0, v26, s[64:65]
	v_cndmask_b32_e64 v27, 0, v27, s[66:67]
	v_mfma_f32_32x32x16_f16 v[56:71], v[192:195], v[220:223], v[56:71]
	v_cvt_pkrtz_f16_f32 v32, v24, v25
	v_cvt_pkrtz_f16_f32 v33, v26, v27
	v_pk_mul_f32 v[24:25], v[16:17], s[36:37] op_sel:[0,1] op_sel_hi:[1,1]
	v_pk_mul_f32 v[26:27], v[18:19], s[36:37] op_sel:[0,1] op_sel_hi:[1,1]
	v_pk_mul_f32 v[28:29], v[20:21], s[44:45] op_sel:[0,1] op_sel_hi:[1,1]
	v_pk_mul_f32 v[30:31], v[22:23], s[44:45] op_sel:[0,1] op_sel_hi:[1,1]
	v_mfma_f32_32x32x16_f16 v[72:87], v[192:195], v[12:15], v[72:87]
	v_cmp_lt_i32_e64 s[60:61], 0, v140
	v_cmp_lt_i32_e64 s[62:63], 0, v141
	v_cmp_lt_i32_e64 s[64:65], 0, v142
	v_cmp_lt_i32_e64 s[66:67], 0, v143
	v_max_f32_e32 v24, v24, v28
	v_max_f32_e32 v25, v25, v29
	v_max_f32_e32 v26, v26, v30
	v_max_f32_e32 v27, v27, v31
	v_cndmask_b32_e64 v24, 0, v24, s[60:61]
	v_cndmask_b32_e64 v25, 0, v25, s[62:63]
	v_cndmask_b32_e64 v26, 0, v26, s[64:65]
	v_cndmask_b32_e64 v27, 0, v27, s[66:67]
	v_mfma_f32_32x32x16_f16 v[40:55], v[196:199], v[224:227], v[40:55]
	v_cvt_pkrtz_f16_f32 v34, v24, v25
	v_cvt_pkrtz_f16_f32 v35, v26, v27
	ds_write2_b64 v6, v[32:33], v[34:35] offset0:0 offset1:66
	v_pk_mul_f32 v[24:25], v[16:17], s[38:39] op_sel_hi:[1,0]
	v_pk_mul_f32 v[26:27], v[18:19], s[38:39] op_sel_hi:[1,0]
	v_pk_mul_f32 v[28:29], v[20:21], s[46:47] op_sel_hi:[1,0]
	v_pk_mul_f32 v[30:31], v[22:23], s[46:47] op_sel_hi:[1,0]
	v_mfma_f32_32x32x16_f16 v[56:71], v[196:199], v[228:231], v[56:71]
	v_cmp_lt_i32_e64 s[60:61], 0, v144
	v_cmp_lt_i32_e64 s[62:63], 0, v145
	v_cmp_lt_i32_e64 s[64:65], 0, v146
	v_cmp_lt_i32_e64 s[66:67], 0, v147
	v_max_f32_e32 v24, v24, v28
	v_max_f32_e32 v25, v25, v29
	v_max_f32_e32 v26, v26, v30
	v_max_f32_e32 v27, v27, v31
	v_cndmask_b32_e64 v24, 0, v24, s[60:61]
	v_cndmask_b32_e64 v25, 0, v25, s[62:63]
	v_cndmask_b32_e64 v26, 0, v26, s[64:65]
	v_cndmask_b32_e64 v27, 0, v27, s[66:67]
	v_cvt_pkrtz_f16_f32 v32, v24, v25
	v_cvt_pkrtz_f16_f32 v33, v26, v27
	v_pk_mul_f32 v[24:25], v[16:17], s[38:39] op_sel:[0,1] op_sel_hi:[1,1]
	v_pk_mul_f32 v[26:27], v[18:19], s[38:39] op_sel:[0,1] op_sel_hi:[1,1]
	v_pk_mul_f32 v[28:29], v[20:21], s[46:47] op_sel:[0,1] op_sel_hi:[1,1]
	v_pk_mul_f32 v[30:31], v[22:23], s[46:47] op_sel:[0,1] op_sel_hi:[1,1]
	v_mfma_f32_32x32x16_f16 v[72:87], v[196:199], v[12:15], v[72:87]
	v_cmp_lt_i32_e64 s[60:61], 0, v148
	v_cmp_lt_i32_e64 s[62:63], 0, v149
	v_cmp_lt_i32_e64 s[64:65], 0, v150
	v_cmp_lt_i32_e64 s[66:67], 0, v151
	v_max_f32_e32 v24, v24, v28
	v_max_f32_e32 v25, v25, v29
	v_max_f32_e32 v26, v26, v30
	v_max_f32_e32 v27, v27, v31
	v_cndmask_b32_e64 v24, 0, v24, s[60:61]
	v_cndmask_b32_e64 v25, 0, v25, s[62:63]
	v_cndmask_b32_e64 v26, 0, v26, s[64:65]
	v_cndmask_b32_e64 v27, 0, v27, s[66:67]
	v_cvt_pkrtz_f16_f32 v34, v24, v25
	v_cvt_pkrtz_f16_f32 v35, v26, v27
	ds_write2_b64 v6, v[32:33], v[34:35] offset0:132 offset1:198
	ds_write_b128 v9, v[168:171] offset:32768
	ds_write_b128 v9, v[172:175] offset:33792
	ds_write_b128 v9, v[176:179] offset:34816
	ds_write_b128 v9, v[180:183] offset:35840
	s_add_u32 s3, s19, 2
	s_and_b32 s3, s3, 7
	s_lshl_b32 s3, s3, 10
	v_add_u32_e32 v11, s3, v10
	ds_read_b128 v[16:19], v11
	ds_read_b128 v[20:23], v11 offset:8192
	s_waitcnt lgkmcnt(0)
	s_barrier
	ds_read_b128 v[184:187], v7 offset:33792
	ds_read_b128 v[200:203], v8 offset:32768
	ds_read_b128 v[204:207], v8 offset:33792
	ds_read_b128 v[188:191], v7 offset:33824
	ds_read_b128 v[208:211], v8 offset:34816
	ds_read_b128 v[212:215], v8 offset:35840
	ds_read_b128 v[192:195], v7 offset:33856
	ds_read_b128 v[216:219], v8 offset:36864
	ds_read_b128 v[220:223], v8 offset:37888
	ds_read_b128 v[196:199], v7 offset:33888
	ds_read_b128 v[224:227], v8 offset:38912
	ds_read_b128 v[228:231], v8 offset:39936
	s_add_u32 s3, s19, 3
	s_and_b32 s3, s3, 7
	s_lshl_b32 s57, s3, 10
	s_add_u32 s48, s57, s22
	s_add_u32 s49, s48, 0x2000
	s_add_u32 s50, s48, 0x4000
	s_add_u32 s51, s48, 0x6000
	s_add_u32 s52, s48, 0x8000
	s_add_u32 s53, s48, 0xa000
	s_add_u32 s54, s48, 0xc000
	s_add_u32 s55, s48, 0xe000
	s_lshl_b32 s56, s3, 15
	s_add_u32 s56, s56, s23
	buffer_load_dwordx4 v[120:123], v1, s[4:7], s48 offen nt
	buffer_load_dwordx4 v[124:127], v1, s[4:7], s49 offen nt
	buffer_load_dwordx4 v[128:131], v1, s[4:7], s50 offen nt
	buffer_load_dwordx4 v[132:135], v1, s[4:7], s51 offen nt
	buffer_load_dwordx4 v[136:139], v1, s[4:7], s52 offen nt
	buffer_load_dwordx4 v[140:143], v1, s[4:7], s53 offen nt
	buffer_load_dwordx4 v[144:147], v1, s[4:7], s54 offen nt
	buffer_load_dwordx4 v[148:151], v1, s[4:7], s55 offen nt
	buffer_load_dwordx4 v[168:171], v1, s[8:11], s56 offen
	buffer_load_dwordx4 v[172:175], v1, s[8:11], s56 offen offset:1024
	buffer_load_dwordx4 v[176:179], v1, s[8:11], s56 offen offset:2048
	buffer_load_dwordx4 v[180:183], v1, s[8:11], s56 offen offset:3072
	s_waitcnt vmcnt(12)
	v_pk_mul_f32 v[24:25], v[16:17], s[32:33] op_sel_hi:[1,0]
	v_pk_mul_f32 v[26:27], v[18:19], s[32:33] op_sel_hi:[1,0]
	v_pk_mul_f32 v[28:29], v[20:21], s[40:41] op_sel_hi:[1,0]
	v_pk_mul_f32 v[30:31], v[22:23], s[40:41] op_sel_hi:[1,0]
	v_cmp_lt_i32_e64 s[60:61], 0, v88
	v_cmp_lt_i32_e64 s[62:63], 0, v89
	v_cmp_lt_i32_e64 s[64:65], 0, v90
	v_cmp_lt_i32_e64 s[66:67], 0, v91
	v_max_f32_e32 v24, v24, v28
	v_max_f32_e32 v25, v25, v29
	v_max_f32_e32 v26, v26, v30
	v_max_f32_e32 v27, v27, v31
	v_cndmask_b32_e64 v24, 0, v24, s[60:61]
	v_cndmask_b32_e64 v25, 0, v25, s[62:63]
	v_cndmask_b32_e64 v26, 0, v26, s[64:65]
	v_cndmask_b32_e64 v27, 0, v27, s[66:67]
	v_cvt_pkrtz_f16_f32 v32, v24, v25
	v_cvt_pkrtz_f16_f32 v33, v26, v27
	s_waitcnt lgkmcnt(0)
	v_pk_mul_f32 v[24:25], v[16:17], s[32:33] op_sel:[0,1] op_sel_hi:[1,1]
	v_pk_mul_f32 v[26:27], v[18:19], s[32:33] op_sel:[0,1] op_sel_hi:[1,1]
	v_pk_mul_f32 v[28:29], v[20:21], s[40:41] op_sel:[0,1] op_sel_hi:[1,1]
	v_pk_mul_f32 v[30:31], v[22:23], s[40:41] op_sel:[0,1] op_sel_hi:[1,1]
	v_mfma_f32_32x32x16_f16 v[40:55], v[184:187], v[200:203], v[40:55]
	v_cmp_lt_i32_e64 s[60:61], 0, v92
	v_cmp_lt_i32_e64 s[62:63], 0, v93
	v_cmp_lt_i32_e64 s[64:65], 0, v94
	v_cmp_lt_i32_e64 s[66:67], 0, v95
	v_max_f32_e32 v24, v24, v28
	v_max_f32_e32 v25, v25, v29
	v_max_f32_e32 v26, v26, v30
	v_max_f32_e32 v27, v27, v31
	v_cndmask_b32_e64 v24, 0, v24, s[60:61]
	v_cndmask_b32_e64 v25, 0, v25, s[62:63]
	v_cndmask_b32_e64 v26, 0, v26, s[64:65]
	v_cndmask_b32_e64 v27, 0, v27, s[66:67]
	v_mfma_f32_32x32x16_f16 v[56:71], v[184:187], v[204:207], v[56:71]
	v_cvt_pkrtz_f16_f32 v34, v24, v25
	v_cvt_pkrtz_f16_f32 v35, v26, v27
	ds_write2_b64 v3, v[32:33], v[34:35] offset0:0 offset1:66
	v_pk_mul_f32 v[24:25], v[16:17], s[34:35] op_sel_hi:[1,0]
	v_pk_mul_f32 v[26:27], v[18:19], s[34:35] op_sel_hi:[1,0]
	v_pk_mul_f32 v[28:29], v[20:21], s[42:43] op_sel_hi:[1,0]
	v_pk_mul_f32 v[30:31], v[22:23], s[42:43] op_sel_hi:[1,0]
	v_mfma_f32_32x32x16_f16 v[72:87], v[184:187], v[12:15], v[72:87]
	v_cmp_lt_i32_e64 s[60:61], 0, v96
	v_cmp_lt_i32_e64 s[62:63], 0, v97
	v_cmp_lt_i32_e64 s[64:65], 0, v98
	v_cmp_lt_i32_e64 s[66:67], 0, v99
	v_max_f32_e32 v24, v24, v28
	v_max_f32_e32 v25, v25, v29
	v_max_f32_e32 v26, v26, v30
	v_max_f32_e32 v27, v27, v31
	v_cndmask_b32_e64 v24, 0, v24, s[60:61]
	v_cndmask_b32_e64 v25, 0, v25, s[62:63]
	v_cndmask_b32_e64 v26, 0, v26, s[64:65]
	v_cndmask_b32_e64 v27, 0, v27, s[66:67]
	v_mfma_f32_32x32x16_f16 v[40:55], v[188:191], v[208:211], v[40:55]
	v_cvt_pkrtz_f16_f32 v32, v24, v25
	v_cvt_pkrtz_f16_f32 v33, v26, v27
	v_pk_mul_f32 v[24:25], v[16:17], s[34:35] op_sel:[0,1] op_sel_hi:[1,1]
	v_pk_mul_f32 v[26:27], v[18:19], s[34:35] op_sel:[0,1] op_sel_hi:[1,1]
	v_pk_mul_f32 v[28:29], v[20:21], s[42:43] op_sel:[0,1] op_sel_hi:[1,1]
	v_pk_mul_f32 v[30:31], v[22:23], s[42:43] op_sel:[0,1] op_sel_hi:[1,1]
	v_mfma_f32_32x32x16_f16 v[56:71], v[188:191], v[212:215], v[56:71]
	v_cmp_lt_i32_e64 s[60:61], 0, v100
	v_cmp_lt_i32_e64 s[62:63], 0, v101
	v_cmp_lt_i32_e64 s[64:65], 0, v102
	v_cmp_lt_i32_e64 s[66:67], 0, v103
	v_max_f32_e32 v24, v24, v28
	v_max_f32_e32 v25, v25, v29
	v_max_f32_e32 v26, v26, v30
	v_max_f32_e32 v27, v27, v31
	v_cndmask_b32_e64 v24, 0, v24, s[60:61]
	v_cndmask_b32_e64 v25, 0, v25, s[62:63]
	v_cndmask_b32_e64 v26, 0, v26, s[64:65]
	v_cndmask_b32_e64 v27, 0, v27, s[66:67]
	v_mfma_f32_32x32x16_f16 v[72:87], v[188:191], v[12:15], v[72:87]
	v_cvt_pkrtz_f16_f32 v34, v24, v25
	v_cvt_pkrtz_f16_f32 v35, v26, v27
	ds_write2_b64 v3, v[32:33], v[34:35] offset0:132 offset1:198
	v_pk_mul_f32 v[24:25], v[16:17], s[36:37] op_sel_hi:[1,0]
	v_pk_mul_f32 v[26:27], v[18:19], s[36:37] op_sel_hi:[1,0]
	v_pk_mul_f32 v[28:29], v[20:21], s[44:45] op_sel_hi:[1,0]
	v_pk_mul_f32 v[30:31], v[22:23], s[44:45] op_sel_hi:[1,0]
	v_mfma_f32_32x32x16_f16 v[40:55], v[192:195], v[216:219], v[40:55]
	v_cmp_lt_i32_e64 s[60:61], 0, v104
	v_cmp_lt_i32_e64 s[62:63], 0, v105
	v_cmp_lt_i32_e64 s[64:65], 0, v106
	v_cmp_lt_i32_e64 s[66:67], 0, v107
	v_max_f32_e32 v24, v24, v28
	v_max_f32_e32 v25, v25, v29
	v_max_f32_e32 v26, v26, v30
	v_max_f32_e32 v27, v27, v31
	v_cndmask_b32_e64 v24, 0, v24, s[60:61]
	v_cndmask_b32_e64 v25, 0, v25, s[62:63]
	v_cndmask_b32_e64 v26, 0, v26, s[64:65]
	v_cndmask_b32_e64 v27, 0, v27, s[66:67]
	v_mfma_f32_32x32x16_f16 v[56:71], v[192:195], v[220:223], v[56:71]
	v_cvt_pkrtz_f16_f32 v32, v24, v25
	v_cvt_pkrtz_f16_f32 v33, v26, v27
	v_pk_mul_f32 v[24:25], v[16:17], s[36:37] op_sel:[0,1] op_sel_hi:[1,1]
	v_pk_mul_f32 v[26:27], v[18:19], s[36:37] op_sel:[0,1] op_sel_hi:[1,1]
	v_pk_mul_f32 v[28:29], v[20:21], s[44:45] op_sel:[0,1] op_sel_hi:[1,1]
	v_pk_mul_f32 v[30:31], v[22:23], s[44:45] op_sel:[0,1] op_sel_hi:[1,1]
	v_mfma_f32_32x32x16_f16 v[72:87], v[192:195], v[12:15], v[72:87]
	v_cmp_lt_i32_e64 s[60:61], 0, v108
	v_cmp_lt_i32_e64 s[62:63], 0, v109
	v_cmp_lt_i32_e64 s[64:65], 0, v110
	v_cmp_lt_i32_e64 s[66:67], 0, v111
	v_max_f32_e32 v24, v24, v28
	v_max_f32_e32 v25, v25, v29
	v_max_f32_e32 v26, v26, v30
	v_max_f32_e32 v27, v27, v31
	v_cndmask_b32_e64 v24, 0, v24, s[60:61]
	v_cndmask_b32_e64 v25, 0, v25, s[62:63]
	v_cndmask_b32_e64 v26, 0, v26, s[64:65]
	v_cndmask_b32_e64 v27, 0, v27, s[66:67]
	v_mfma_f32_32x32x16_f16 v[40:55], v[196:199], v[224:227], v[40:55]
	v_cvt_pkrtz_f16_f32 v34, v24, v25
	v_cvt_pkrtz_f16_f32 v35, v26, v27
	ds_write2_b64 v4, v[32:33], v[34:35] offset0:0 offset1:66
	v_pk_mul_f32 v[24:25], v[16:17], s[38:39] op_sel_hi:[1,0]
	v_pk_mul_f32 v[26:27], v[18:19], s[38:39] op_sel_hi:[1,0]
	v_pk_mul_f32 v[28:29], v[20:21], s[46:47] op_sel_hi:[1,0]
	v_pk_mul_f32 v[30:31], v[22:23], s[46:47] op_sel_hi:[1,0]
	v_mfma_f32_32x32x16_f16 v[56:71], v[196:199], v[228:231], v[56:71]
	v_cmp_lt_i32_e64 s[60:61], 0, v112
	v_cmp_lt_i32_e64 s[62:63], 0, v113
	v_cmp_lt_i32_e64 s[64:65], 0, v114
	v_cmp_lt_i32_e64 s[66:67], 0, v115
	v_max_f32_e32 v24, v24, v28
	v_max_f32_e32 v25, v25, v29
	v_max_f32_e32 v26, v26, v30
	v_max_f32_e32 v27, v27, v31
	v_cndmask_b32_e64 v24, 0, v24, s[60:61]
	v_cndmask_b32_e64 v25, 0, v25, s[62:63]
	v_cndmask_b32_e64 v26, 0, v26, s[64:65]
	v_cndmask_b32_e64 v27, 0, v27, s[66:67]
	v_cvt_pkrtz_f16_f32 v32, v24, v25
	v_cvt_pkrtz_f16_f32 v33, v26, v27
	v_pk_mul_f32 v[24:25], v[16:17], s[38:39] op_sel:[0,1] op_sel_hi:[1,1]
	v_pk_mul_f32 v[26:27], v[18:19], s[38:39] op_sel:[0,1] op_sel_hi:[1,1]
	v_pk_mul_f32 v[28:29], v[20:21], s[46:47] op_sel:[0,1] op_sel_hi:[1,1]
	v_pk_mul_f32 v[30:31], v[22:23], s[46:47] op_sel:[0,1] op_sel_hi:[1,1]
	v_mfma_f32_32x32x16_f16 v[72:87], v[196:199], v[12:15], v[72:87]
	v_cmp_lt_i32_e64 s[60:61], 0, v116
	v_cmp_lt_i32_e64 s[62:63], 0, v117
	v_cmp_lt_i32_e64 s[64:65], 0, v118
	v_cmp_lt_i32_e64 s[66:67], 0, v119
	v_max_f32_e32 v24, v24, v28
	v_max_f32_e32 v25, v25, v29
	v_max_f32_e32 v26, v26, v30
	v_max_f32_e32 v27, v27, v31
	v_cndmask_b32_e64 v24, 0, v24, s[60:61]
	v_cndmask_b32_e64 v25, 0, v25, s[62:63]
	v_cndmask_b32_e64 v26, 0, v26, s[64:65]
	v_cndmask_b32_e64 v27, 0, v27, s[66:67]
	v_cvt_pkrtz_f16_f32 v34, v24, v25
	v_cvt_pkrtz_f16_f32 v35, v26, v27
	ds_write2_b64 v4, v[32:33], v[34:35] offset0:132 offset1:198
	ds_write_b128 v9, v[152:155] offset:0
	ds_write_b128 v9, v[156:159] offset:1024
	ds_write_b128 v9, v[160:163] offset:2048
	ds_write_b128 v9, v[164:167] offset:3072
	s_add_u32 s3, s19, 3
	s_and_b32 s3, s3, 7
	s_lshl_b32 s3, s3, 10
	v_add_u32_e32 v11, s3, v10
	ds_read_b128 v[16:19], v11
	ds_read_b128 v[20:23], v11 offset:8192
	s_waitcnt lgkmcnt(0)
	s_barrier
	ds_read_b128 v[184:187], v7 offset:0
	ds_read_b128 v[200:203], v8 offset:0
	ds_read_b128 v[204:207], v8 offset:1024
	ds_read_b128 v[188:191], v7 offset:32
	ds_read_b128 v[208:211], v8 offset:2048
	ds_read_b128 v[212:215], v8 offset:3072
	ds_read_b128 v[192:195], v7 offset:64
	ds_read_b128 v[216:219], v8 offset:4096
	ds_read_b128 v[220:223], v8 offset:5120
	ds_read_b128 v[196:199], v7 offset:96
	ds_read_b128 v[224:227], v8 offset:6144
	ds_read_b128 v[228:231], v8 offset:7168
	s_add_u32 s3, s19, 4
	s_and_b32 s3, s3, 7
	s_lshl_b32 s57, s3, 10
	s_add_u32 s48, s57, s22
	s_add_u32 s49, s48, 0x2000
	s_add_u32 s50, s48, 0x4000
	s_add_u32 s51, s48, 0x6000
	s_add_u32 s52, s48, 0x8000
	s_add_u32 s53, s48, 0xa000
	s_add_u32 s54, s48, 0xc000
	s_add_u32 s55, s48, 0xe000
	s_lshl_b32 s56, s3, 15
	s_add_u32 s56, s56, s23
	buffer_load_dwordx4 v[88:91], v1, s[4:7], s48 offen nt
	buffer_load_dwordx4 v[92:95], v1, s[4:7], s49 offen nt
	buffer_load_dwordx4 v[96:99], v1, s[4:7], s50 offen nt
	buffer_load_dwordx4 v[100:103], v1, s[4:7], s51 offen nt
	buffer_load_dwordx4 v[104:107], v1, s[4:7], s52 offen nt
	buffer_load_dwordx4 v[108:111], v1, s[4:7], s53 offen nt
	buffer_load_dwordx4 v[112:115], v1, s[4:7], s54 offen nt
	buffer_load_dwordx4 v[116:119], v1, s[4:7], s55 offen nt
	buffer_load_dwordx4 v[152:155], v1, s[8:11], s56 offen
	buffer_load_dwordx4 v[156:159], v1, s[8:11], s56 offen offset:1024
	buffer_load_dwordx4 v[160:163], v1, s[8:11], s56 offen offset:2048
	buffer_load_dwordx4 v[164:167], v1, s[8:11], s56 offen offset:3072
	s_waitcnt vmcnt(12)
	v_pk_mul_f32 v[24:25], v[16:17], s[32:33] op_sel_hi:[1,0]
	v_pk_mul_f32 v[26:27], v[18:19], s[32:33] op_sel_hi:[1,0]
	v_pk_mul_f32 v[28:29], v[20:21], s[40:41] op_sel_hi:[1,0]
	v_pk_mul_f32 v[30:31], v[22:23], s[40:41] op_sel_hi:[1,0]
	v_cmp_lt_i32_e64 s[60:61], 0, v120
	v_cmp_lt_i32_e64 s[62:63], 0, v121
	v_cmp_lt_i32_e64 s[64:65], 0, v122
	v_cmp_lt_i32_e64 s[66:67], 0, v123
	v_max_f32_e32 v24, v24, v28
	v_max_f32_e32 v25, v25, v29
	v_max_f32_e32 v26, v26, v30
	v_max_f32_e32 v27, v27, v31
	v_cndmask_b32_e64 v24, 0, v24, s[60:61]
	v_cndmask_b32_e64 v25, 0, v25, s[62:63]
	v_cndmask_b32_e64 v26, 0, v26, s[64:65]
	v_cndmask_b32_e64 v27, 0, v27, s[66:67]
	v_cvt_pkrtz_f16_f32 v32, v24, v25
	v_cvt_pkrtz_f16_f32 v33, v26, v27
	s_waitcnt lgkmcnt(0)
	v_pk_mul_f32 v[24:25], v[16:17], s[32:33] op_sel:[0,1] op_sel_hi:[1,1]
	v_pk_mul_f32 v[26:27], v[18:19], s[32:33] op_sel:[0,1] op_sel_hi:[1,1]
	v_pk_mul_f32 v[28:29], v[20:21], s[40:41] op_sel:[0,1] op_sel_hi:[1,1]
	v_pk_mul_f32 v[30:31], v[22:23], s[40:41] op_sel:[0,1] op_sel_hi:[1,1]
	v_mfma_f32_32x32x16_f16 v[40:55], v[184:187], v[200:203], v[40:55]
	v_cmp_lt_i32_e64 s[60:61], 0, v124
	v_cmp_lt_i32_e64 s[62:63], 0, v125
	v_cmp_lt_i32_e64 s[64:65], 0, v126
	v_cmp_lt_i32_e64 s[66:67], 0, v127
	v_max_f32_e32 v24, v24, v28
	v_max_f32_e32 v25, v25, v29
	v_max_f32_e32 v26, v26, v30
	v_max_f32_e32 v27, v27, v31
	v_cndmask_b32_e64 v24, 0, v24, s[60:61]
	v_cndmask_b32_e64 v25, 0, v25, s[62:63]
	v_cndmask_b32_e64 v26, 0, v26, s[64:65]
	v_cndmask_b32_e64 v27, 0, v27, s[66:67]
	v_mfma_f32_32x32x16_f16 v[56:71], v[184:187], v[204:207], v[56:71]
	v_cvt_pkrtz_f16_f32 v34, v24, v25
	v_cvt_pkrtz_f16_f32 v35, v26, v27
	ds_write2_b64 v5, v[32:33], v[34:35] offset0:0 offset1:66
	v_pk_mul_f32 v[24:25], v[16:17], s[34:35] op_sel_hi:[1,0]
	v_pk_mul_f32 v[26:27], v[18:19], s[34:35] op_sel_hi:[1,0]
	v_pk_mul_f32 v[28:29], v[20:21], s[42:43] op_sel_hi:[1,0]
	v_pk_mul_f32 v[30:31], v[22:23], s[42:43] op_sel_hi:[1,0]
	v_mfma_f32_32x32x16_f16 v[72:87], v[184:187], v[12:15], v[72:87]
	v_cmp_lt_i32_e64 s[60:61], 0, v128
	v_cmp_lt_i32_e64 s[62:63], 0, v129
	v_cmp_lt_i32_e64 s[64:65], 0, v130
	v_cmp_lt_i32_e64 s[66:67], 0, v131
	v_max_f32_e32 v24, v24, v28
	v_max_f32_e32 v25, v25, v29
	v_max_f32_e32 v26, v26, v30
	v_max_f32_e32 v27, v27, v31
	v_cndmask_b32_e64 v24, 0, v24, s[60:61]
	v_cndmask_b32_e64 v25, 0, v25, s[62:63]
	v_cndmask_b32_e64 v26, 0, v26, s[64:65]
	v_cndmask_b32_e64 v27, 0, v27, s[66:67]
	v_mfma_f32_32x32x16_f16 v[40:55], v[188:191], v[208:211], v[40:55]
	v_cvt_pkrtz_f16_f32 v32, v24, v25
	v_cvt_pkrtz_f16_f32 v33, v26, v27
	v_pk_mul_f32 v[24:25], v[16:17], s[34:35] op_sel:[0,1] op_sel_hi:[1,1]
	v_pk_mul_f32 v[26:27], v[18:19], s[34:35] op_sel:[0,1] op_sel_hi:[1,1]
	v_pk_mul_f32 v[28:29], v[20:21], s[42:43] op_sel:[0,1] op_sel_hi:[1,1]
	v_pk_mul_f32 v[30:31], v[22:23], s[42:43] op_sel:[0,1] op_sel_hi:[1,1]
	v_mfma_f32_32x32x16_f16 v[56:71], v[188:191], v[212:215], v[56:71]
	v_cmp_lt_i32_e64 s[60:61], 0, v132
	v_cmp_lt_i32_e64 s[62:63], 0, v133
	v_cmp_lt_i32_e64 s[64:65], 0, v134
	v_cmp_lt_i32_e64 s[66:67], 0, v135
	v_max_f32_e32 v24, v24, v28
	v_max_f32_e32 v25, v25, v29
	v_max_f32_e32 v26, v26, v30
	v_max_f32_e32 v27, v27, v31
	v_cndmask_b32_e64 v24, 0, v24, s[60:61]
	v_cndmask_b32_e64 v25, 0, v25, s[62:63]
	v_cndmask_b32_e64 v26, 0, v26, s[64:65]
	v_cndmask_b32_e64 v27, 0, v27, s[66:67]
	v_mfma_f32_32x32x16_f16 v[72:87], v[188:191], v[12:15], v[72:87]
	v_cvt_pkrtz_f16_f32 v34, v24, v25
	v_cvt_pkrtz_f16_f32 v35, v26, v27
	ds_write2_b64 v5, v[32:33], v[34:35] offset0:132 offset1:198
	v_pk_mul_f32 v[24:25], v[16:17], s[36:37] op_sel_hi:[1,0]
	v_pk_mul_f32 v[26:27], v[18:19], s[36:37] op_sel_hi:[1,0]
	v_pk_mul_f32 v[28:29], v[20:21], s[44:45] op_sel_hi:[1,0]
	v_pk_mul_f32 v[30:31], v[22:23], s[44:45] op_sel_hi:[1,0]
	v_mfma_f32_32x32x16_f16 v[40:55], v[192:195], v[216:219], v[40:55]
	v_cmp_lt_i32_e64 s[60:61], 0, v136
	v_cmp_lt_i32_e64 s[62:63], 0, v137
	v_cmp_lt_i32_e64 s[64:65], 0, v138
	v_cmp_lt_i32_e64 s[66:67], 0, v139
	v_max_f32_e32 v24, v24, v28
	v_max_f32_e32 v25, v25, v29
	v_max_f32_e32 v26, v26, v30
	v_max_f32_e32 v27, v27, v31
	v_cndmask_b32_e64 v24, 0, v24, s[60:61]
	v_cndmask_b32_e64 v25, 0, v25, s[62:63]
	v_cndmask_b32_e64 v26, 0, v26, s[64:65]
	v_cndmask_b32_e64 v27, 0, v27, s[66:67]
	v_mfma_f32_32x32x16_f16 v[56:71], v[192:195], v[220:223], v[56:71]
	v_cvt_pkrtz_f16_f32 v32, v24, v25
	v_cvt_pkrtz_f16_f32 v33, v26, v27
	v_pk_mul_f32 v[24:25], v[16:17], s[36:37] op_sel:[0,1] op_sel_hi:[1,1]
	v_pk_mul_f32 v[26:27], v[18:19], s[36:37] op_sel:[0,1] op_sel_hi:[1,1]
	v_pk_mul_f32 v[28:29], v[20:21], s[44:45] op_sel:[0,1] op_sel_hi:[1,1]
	v_pk_mul_f32 v[30:31], v[22:23], s[44:45] op_sel:[0,1] op_sel_hi:[1,1]
	v_mfma_f32_32x32x16_f16 v[72:87], v[192:195], v[12:15], v[72:87]
	v_cmp_lt_i32_e64 s[60:61], 0, v140
	v_cmp_lt_i32_e64 s[62:63], 0, v141
	v_cmp_lt_i32_e64 s[64:65], 0, v142
	v_cmp_lt_i32_e64 s[66:67], 0, v143
	v_max_f32_e32 v24, v24, v28
	v_max_f32_e32 v25, v25, v29
	v_max_f32_e32 v26, v26, v30
	v_max_f32_e32 v27, v27, v31
	v_cndmask_b32_e64 v24, 0, v24, s[60:61]
	v_cndmask_b32_e64 v25, 0, v25, s[62:63]
	v_cndmask_b32_e64 v26, 0, v26, s[64:65]
	v_cndmask_b32_e64 v27, 0, v27, s[66:67]
	v_mfma_f32_32x32x16_f16 v[40:55], v[196:199], v[224:227], v[40:55]
	v_cvt_pkrtz_f16_f32 v34, v24, v25
	v_cvt_pkrtz_f16_f32 v35, v26, v27
	ds_write2_b64 v6, v[32:33], v[34:35] offset0:0 offset1:66
	v_pk_mul_f32 v[24:25], v[16:17], s[38:39] op_sel_hi:[1,0]
	v_pk_mul_f32 v[26:27], v[18:19], s[38:39] op_sel_hi:[1,0]
	v_pk_mul_f32 v[28:29], v[20:21], s[46:47] op_sel_hi:[1,0]
	v_pk_mul_f32 v[30:31], v[22:23], s[46:47] op_sel_hi:[1,0]
	v_mfma_f32_32x32x16_f16 v[56:71], v[196:199], v[228:231], v[56:71]
	v_cmp_lt_i32_e64 s[60:61], 0, v144
	v_cmp_lt_i32_e64 s[62:63], 0, v145
	v_cmp_lt_i32_e64 s[64:65], 0, v146
	v_cmp_lt_i32_e64 s[66:67], 0, v147
	v_max_f32_e32 v24, v24, v28
	v_max_f32_e32 v25, v25, v29
	v_max_f32_e32 v26, v26, v30
	v_max_f32_e32 v27, v27, v31
	v_cndmask_b32_e64 v24, 0, v24, s[60:61]
	v_cndmask_b32_e64 v25, 0, v25, s[62:63]
	v_cndmask_b32_e64 v26, 0, v26, s[64:65]
	v_cndmask_b32_e64 v27, 0, v27, s[66:67]
	v_cvt_pkrtz_f16_f32 v32, v24, v25
	v_cvt_pkrtz_f16_f32 v33, v26, v27
	v_pk_mul_f32 v[24:25], v[16:17], s[38:39] op_sel:[0,1] op_sel_hi:[1,1]
	v_pk_mul_f32 v[26:27], v[18:19], s[38:39] op_sel:[0,1] op_sel_hi:[1,1]
	v_pk_mul_f32 v[28:29], v[20:21], s[46:47] op_sel:[0,1] op_sel_hi:[1,1]
	v_pk_mul_f32 v[30:31], v[22:23], s[46:47] op_sel:[0,1] op_sel_hi:[1,1]
	v_mfma_f32_32x32x16_f16 v[72:87], v[196:199], v[12:15], v[72:87]
	v_cmp_lt_i32_e64 s[60:61], 0, v148
	v_cmp_lt_i32_e64 s[62:63], 0, v149
	v_cmp_lt_i32_e64 s[64:65], 0, v150
	v_cmp_lt_i32_e64 s[66:67], 0, v151
	v_max_f32_e32 v24, v24, v28
	v_max_f32_e32 v25, v25, v29
	v_max_f32_e32 v26, v26, v30
	v_max_f32_e32 v27, v27, v31
	v_cndmask_b32_e64 v24, 0, v24, s[60:61]
	v_cndmask_b32_e64 v25, 0, v25, s[62:63]
	v_cndmask_b32_e64 v26, 0, v26, s[64:65]
	v_cndmask_b32_e64 v27, 0, v27, s[66:67]
	v_cvt_pkrtz_f16_f32 v34, v24, v25
	v_cvt_pkrtz_f16_f32 v35, v26, v27
	ds_write2_b64 v6, v[32:33], v[34:35] offset0:132 offset1:198
	ds_write_b128 v9, v[168:171] offset:32768
	ds_write_b128 v9, v[172:175] offset:33792
	ds_write_b128 v9, v[176:179] offset:34816
	ds_write_b128 v9, v[180:183] offset:35840
	s_add_u32 s3, s19, 4
	s_and_b32 s3, s3, 7
	s_lshl_b32 s3, s3, 10
	v_add_u32_e32 v11, s3, v10
	ds_read_b128 v[16:19], v11
	ds_read_b128 v[20:23], v11 offset:8192
	s_waitcnt lgkmcnt(0)
	s_barrier
	ds_read_b128 v[184:187], v7 offset:33792
	ds_read_b128 v[200:203], v8 offset:32768
	ds_read_b128 v[204:207], v8 offset:33792
	ds_read_b128 v[188:191], v7 offset:33824
	ds_read_b128 v[208:211], v8 offset:34816
	ds_read_b128 v[212:215], v8 offset:35840
	ds_read_b128 v[192:195], v7 offset:33856
	ds_read_b128 v[216:219], v8 offset:36864
	ds_read_b128 v[220:223], v8 offset:37888
	ds_read_b128 v[196:199], v7 offset:33888
	ds_read_b128 v[224:227], v8 offset:38912
	ds_read_b128 v[228:231], v8 offset:39936
	s_add_u32 s3, s19, 5
	s_and_b32 s3, s3, 7
	s_lshl_b32 s57, s3, 10
	s_add_u32 s48, s57, s22
	s_add_u32 s49, s48, 0x2000
	s_add_u32 s50, s48, 0x4000
	s_add_u32 s51, s48, 0x6000
	s_add_u32 s52, s48, 0x8000
	s_add_u32 s53, s48, 0xa000
	s_add_u32 s54, s48, 0xc000
	s_add_u32 s55, s48, 0xe000
	s_lshl_b32 s56, s3, 15
	s_add_u32 s56, s56, s23
	buffer_load_dwordx4 v[120:123], v1, s[4:7], s48 offen nt
	buffer_load_dwordx4 v[124:127], v1, s[4:7], s49 offen nt
	buffer_load_dwordx4 v[128:131], v1, s[4:7], s50 offen nt
	buffer_load_dwordx4 v[132:135], v1, s[4:7], s51 offen nt
	buffer_load_dwordx4 v[136:139], v1, s[4:7], s52 offen nt
	buffer_load_dwordx4 v[140:143], v1, s[4:7], s53 offen nt
	buffer_load_dwordx4 v[144:147], v1, s[4:7], s54 offen nt
	buffer_load_dwordx4 v[148:151], v1, s[4:7], s55 offen nt
	buffer_load_dwordx4 v[168:171], v1, s[8:11], s56 offen
	buffer_load_dwordx4 v[172:175], v1, s[8:11], s56 offen offset:1024
	buffer_load_dwordx4 v[176:179], v1, s[8:11], s56 offen offset:2048
	buffer_load_dwordx4 v[180:183], v1, s[8:11], s56 offen offset:3072
	s_waitcnt vmcnt(12)
	v_pk_mul_f32 v[24:25], v[16:17], s[32:33] op_sel_hi:[1,0]
	v_pk_mul_f32 v[26:27], v[18:19], s[32:33] op_sel_hi:[1,0]
	v_pk_mul_f32 v[28:29], v[20:21], s[40:41] op_sel_hi:[1,0]
	v_pk_mul_f32 v[30:31], v[22:23], s[40:41] op_sel_hi:[1,0]
	v_cmp_lt_i32_e64 s[60:61], 0, v88
	v_cmp_lt_i32_e64 s[62:63], 0, v89
	v_cmp_lt_i32_e64 s[64:65], 0, v90
	v_cmp_lt_i32_e64 s[66:67], 0, v91
	v_max_f32_e32 v24, v24, v28
	v_max_f32_e32 v25, v25, v29
	v_max_f32_e32 v26, v26, v30
	v_max_f32_e32 v27, v27, v31
	v_cndmask_b32_e64 v24, 0, v24, s[60:61]
	v_cndmask_b32_e64 v25, 0, v25, s[62:63]
	v_cndmask_b32_e64 v26, 0, v26, s[64:65]
	v_cndmask_b32_e64 v27, 0, v27, s[66:67]
	v_cvt_pkrtz_f16_f32 v32, v24, v25
	v_cvt_pkrtz_f16_f32 v33, v26, v27
	s_waitcnt lgkmcnt(0)
	v_pk_mul_f32 v[24:25], v[16:17], s[32:33] op_sel:[0,1] op_sel_hi:[1,1]
	v_pk_mul_f32 v[26:27], v[18:19], s[32:33] op_sel:[0,1] op_sel_hi:[1,1]
	v_pk_mul_f32 v[28:29], v[20:21], s[40:41] op_sel:[0,1] op_sel_hi:[1,1]
	v_pk_mul_f32 v[30:31], v[22:23], s[40:41] op_sel:[0,1] op_sel_hi:[1,1]
	v_mfma_f32_32x32x16_f16 v[40:55], v[184:187], v[200:203], v[40:55]
	v_cmp_lt_i32_e64 s[60:61], 0, v92
	v_cmp_lt_i32_e64 s[62:63], 0, v93
	v_cmp_lt_i32_e64 s[64:65], 0, v94
	v_cmp_lt_i32_e64 s[66:67], 0, v95
	v_max_f32_e32 v24, v24, v28
	v_max_f32_e32 v25, v25, v29
	v_max_f32_e32 v26, v26, v30
	v_max_f32_e32 v27, v27, v31
	v_cndmask_b32_e64 v24, 0, v24, s[60:61]
	v_cndmask_b32_e64 v25, 0, v25, s[62:63]
	v_cndmask_b32_e64 v26, 0, v26, s[64:65]
	v_cndmask_b32_e64 v27, 0, v27, s[66:67]
	v_mfma_f32_32x32x16_f16 v[56:71], v[184:187], v[204:207], v[56:71]
	v_cvt_pkrtz_f16_f32 v34, v24, v25
	v_cvt_pkrtz_f16_f32 v35, v26, v27
	ds_write2_b64 v3, v[32:33], v[34:35] offset0:0 offset1:66
	v_pk_mul_f32 v[24:25], v[16:17], s[34:35] op_sel_hi:[1,0]
	v_pk_mul_f32 v[26:27], v[18:19], s[34:35] op_sel_hi:[1,0]
	v_pk_mul_f32 v[28:29], v[20:21], s[42:43] op_sel_hi:[1,0]
	v_pk_mul_f32 v[30:31], v[22:23], s[42:43] op_sel_hi:[1,0]
	v_mfma_f32_32x32x16_f16 v[72:87], v[184:187], v[12:15], v[72:87]
	v_cmp_lt_i32_e64 s[60:61], 0, v96
	v_cmp_lt_i32_e64 s[62:63], 0, v97
	v_cmp_lt_i32_e64 s[64:65], 0, v98
	v_cmp_lt_i32_e64 s[66:67], 0, v99
	v_max_f32_e32 v24, v24, v28
	v_max_f32_e32 v25, v25, v29
	v_max_f32_e32 v26, v26, v30
	v_max_f32_e32 v27, v27, v31
	v_cndmask_b32_e64 v24, 0, v24, s[60:61]
	v_cndmask_b32_e64 v25, 0, v25, s[62:63]
	v_cndmask_b32_e64 v26, 0, v26, s[64:65]
	v_cndmask_b32_e64 v27, 0, v27, s[66:67]
	v_mfma_f32_32x32x16_f16 v[40:55], v[188:191], v[208:211], v[40:55]
	v_cvt_pkrtz_f16_f32 v32, v24, v25
	v_cvt_pkrtz_f16_f32 v33, v26, v27
	v_pk_mul_f32 v[24:25], v[16:17], s[34:35] op_sel:[0,1] op_sel_hi:[1,1]
	v_pk_mul_f32 v[26:27], v[18:19], s[34:35] op_sel:[0,1] op_sel_hi:[1,1]
	v_pk_mul_f32 v[28:29], v[20:21], s[42:43] op_sel:[0,1] op_sel_hi:[1,1]
	v_pk_mul_f32 v[30:31], v[22:23], s[42:43] op_sel:[0,1] op_sel_hi:[1,1]
	v_mfma_f32_32x32x16_f16 v[56:71], v[188:191], v[212:215], v[56:71]
	v_cmp_lt_i32_e64 s[60:61], 0, v100
	v_cmp_lt_i32_e64 s[62:63], 0, v101
	v_cmp_lt_i32_e64 s[64:65], 0, v102
	v_cmp_lt_i32_e64 s[66:67], 0, v103
	v_max_f32_e32 v24, v24, v28
	v_max_f32_e32 v25, v25, v29
	v_max_f32_e32 v26, v26, v30
	v_max_f32_e32 v27, v27, v31
	v_cndmask_b32_e64 v24, 0, v24, s[60:61]
	v_cndmask_b32_e64 v25, 0, v25, s[62:63]
	v_cndmask_b32_e64 v26, 0, v26, s[64:65]
	v_cndmask_b32_e64 v27, 0, v27, s[66:67]
	v_mfma_f32_32x32x16_f16 v[72:87], v[188:191], v[12:15], v[72:87]
	v_cvt_pkrtz_f16_f32 v34, v24, v25
	v_cvt_pkrtz_f16_f32 v35, v26, v27
	ds_write2_b64 v3, v[32:33], v[34:35] offset0:132 offset1:198
	v_pk_mul_f32 v[24:25], v[16:17], s[36:37] op_sel_hi:[1,0]
	v_pk_mul_f32 v[26:27], v[18:19], s[36:37] op_sel_hi:[1,0]
	v_pk_mul_f32 v[28:29], v[20:21], s[44:45] op_sel_hi:[1,0]
	v_pk_mul_f32 v[30:31], v[22:23], s[44:45] op_sel_hi:[1,0]
	v_mfma_f32_32x32x16_f16 v[40:55], v[192:195], v[216:219], v[40:55]
	v_cmp_lt_i32_e64 s[60:61], 0, v104
	v_cmp_lt_i32_e64 s[62:63], 0, v105
	v_cmp_lt_i32_e64 s[64:65], 0, v106
	v_cmp_lt_i32_e64 s[66:67], 0, v107
	v_max_f32_e32 v24, v24, v28
	v_max_f32_e32 v25, v25, v29
	v_max_f32_e32 v26, v26, v30
	v_max_f32_e32 v27, v27, v31
	v_cndmask_b32_e64 v24, 0, v24, s[60:61]
	v_cndmask_b32_e64 v25, 0, v25, s[62:63]
	v_cndmask_b32_e64 v26, 0, v26, s[64:65]
	v_cndmask_b32_e64 v27, 0, v27, s[66:67]
	v_mfma_f32_32x32x16_f16 v[56:71], v[192:195], v[220:223], v[56:71]
	v_cvt_pkrtz_f16_f32 v32, v24, v25
	v_cvt_pkrtz_f16_f32 v33, v26, v27
	v_pk_mul_f32 v[24:25], v[16:17], s[36:37] op_sel:[0,1] op_sel_hi:[1,1]
	v_pk_mul_f32 v[26:27], v[18:19], s[36:37] op_sel:[0,1] op_sel_hi:[1,1]
	v_pk_mul_f32 v[28:29], v[20:21], s[44:45] op_sel:[0,1] op_sel_hi:[1,1]
	v_pk_mul_f32 v[30:31], v[22:23], s[44:45] op_sel:[0,1] op_sel_hi:[1,1]
	v_mfma_f32_32x32x16_f16 v[72:87], v[192:195], v[12:15], v[72:87]
	v_cmp_lt_i32_e64 s[60:61], 0, v108
	v_cmp_lt_i32_e64 s[62:63], 0, v109
	v_cmp_lt_i32_e64 s[64:65], 0, v110
	v_cmp_lt_i32_e64 s[66:67], 0, v111
	v_max_f32_e32 v24, v24, v28
	v_max_f32_e32 v25, v25, v29
	v_max_f32_e32 v26, v26, v30
	v_max_f32_e32 v27, v27, v31
	v_cndmask_b32_e64 v24, 0, v24, s[60:61]
	v_cndmask_b32_e64 v25, 0, v25, s[62:63]
	v_cndmask_b32_e64 v26, 0, v26, s[64:65]
	v_cndmask_b32_e64 v27, 0, v27, s[66:67]
	v_mfma_f32_32x32x16_f16 v[40:55], v[196:199], v[224:227], v[40:55]
	v_cvt_pkrtz_f16_f32 v34, v24, v25
	v_cvt_pkrtz_f16_f32 v35, v26, v27
	ds_write2_b64 v4, v[32:33], v[34:35] offset0:0 offset1:66
	v_pk_mul_f32 v[24:25], v[16:17], s[38:39] op_sel_hi:[1,0]
	v_pk_mul_f32 v[26:27], v[18:19], s[38:39] op_sel_hi:[1,0]
	v_pk_mul_f32 v[28:29], v[20:21], s[46:47] op_sel_hi:[1,0]
	v_pk_mul_f32 v[30:31], v[22:23], s[46:47] op_sel_hi:[1,0]
	v_mfma_f32_32x32x16_f16 v[56:71], v[196:199], v[228:231], v[56:71]
	v_cmp_lt_i32_e64 s[60:61], 0, v112
	v_cmp_lt_i32_e64 s[62:63], 0, v113
	v_cmp_lt_i32_e64 s[64:65], 0, v114
	v_cmp_lt_i32_e64 s[66:67], 0, v115
	v_max_f32_e32 v24, v24, v28
	v_max_f32_e32 v25, v25, v29
	v_max_f32_e32 v26, v26, v30
	v_max_f32_e32 v27, v27, v31
	v_cndmask_b32_e64 v24, 0, v24, s[60:61]
	v_cndmask_b32_e64 v25, 0, v25, s[62:63]
	v_cndmask_b32_e64 v26, 0, v26, s[64:65]
	v_cndmask_b32_e64 v27, 0, v27, s[66:67]
	v_cvt_pkrtz_f16_f32 v32, v24, v25
	v_cvt_pkrtz_f16_f32 v33, v26, v27
	v_pk_mul_f32 v[24:25], v[16:17], s[38:39] op_sel:[0,1] op_sel_hi:[1,1]
	v_pk_mul_f32 v[26:27], v[18:19], s[38:39] op_sel:[0,1] op_sel_hi:[1,1]
	v_pk_mul_f32 v[28:29], v[20:21], s[46:47] op_sel:[0,1] op_sel_hi:[1,1]
	v_pk_mul_f32 v[30:31], v[22:23], s[46:47] op_sel:[0,1] op_sel_hi:[1,1]
	v_mfma_f32_32x32x16_f16 v[72:87], v[196:199], v[12:15], v[72:87]
	v_cmp_lt_i32_e64 s[60:61], 0, v116
	v_cmp_lt_i32_e64 s[62:63], 0, v117
	v_cmp_lt_i32_e64 s[64:65], 0, v118
	v_cmp_lt_i32_e64 s[66:67], 0, v119
	v_max_f32_e32 v24, v24, v28
	v_max_f32_e32 v25, v25, v29
	v_max_f32_e32 v26, v26, v30
	v_max_f32_e32 v27, v27, v31
	v_cndmask_b32_e64 v24, 0, v24, s[60:61]
	v_cndmask_b32_e64 v25, 0, v25, s[62:63]
	v_cndmask_b32_e64 v26, 0, v26, s[64:65]
	v_cndmask_b32_e64 v27, 0, v27, s[66:67]
	v_cvt_pkrtz_f16_f32 v34, v24, v25
	v_cvt_pkrtz_f16_f32 v35, v26, v27
	ds_write2_b64 v4, v[32:33], v[34:35] offset0:132 offset1:198
	ds_write_b128 v9, v[152:155] offset:0
	ds_write_b128 v9, v[156:159] offset:1024
	ds_write_b128 v9, v[160:163] offset:2048
	ds_write_b128 v9, v[164:167] offset:3072
	s_add_u32 s3, s19, 5
	s_and_b32 s3, s3, 7
	s_lshl_b32 s3, s3, 10
	v_add_u32_e32 v11, s3, v10
	ds_read_b128 v[16:19], v11
	ds_read_b128 v[20:23], v11 offset:8192
	s_waitcnt lgkmcnt(0)
	s_barrier
	ds_read_b128 v[184:187], v7 offset:0
	ds_read_b128 v[200:203], v8 offset:0
	ds_read_b128 v[204:207], v8 offset:1024
	ds_read_b128 v[188:191], v7 offset:32
	ds_read_b128 v[208:211], v8 offset:2048
	ds_read_b128 v[212:215], v8 offset:3072
	ds_read_b128 v[192:195], v7 offset:64
	ds_read_b128 v[216:219], v8 offset:4096
	ds_read_b128 v[220:223], v8 offset:5120
	ds_read_b128 v[196:199], v7 offset:96
	ds_read_b128 v[224:227], v8 offset:6144
	ds_read_b128 v[228:231], v8 offset:7168
	s_add_u32 s3, s19, 6
	s_and_b32 s3, s3, 7
	s_lshl_b32 s57, s3, 10
	s_add_u32 s48, s57, s22
	s_add_u32 s49, s48, 0x2000
	s_add_u32 s50, s48, 0x4000
	s_add_u32 s51, s48, 0x6000
	s_add_u32 s52, s48, 0x8000
	s_add_u32 s53, s48, 0xa000
	s_add_u32 s54, s48, 0xc000
	s_add_u32 s55, s48, 0xe000
	s_lshl_b32 s56, s3, 15
	s_add_u32 s56, s56, s23
	buffer_load_dwordx4 v[88:91], v1, s[4:7], s48 offen nt
	buffer_load_dwordx4 v[92:95], v1, s[4:7], s49 offen nt
	buffer_load_dwordx4 v[96:99], v1, s[4:7], s50 offen nt
	buffer_load_dwordx4 v[100:103], v1, s[4:7], s51 offen nt
	buffer_load_dwordx4 v[104:107], v1, s[4:7], s52 offen nt
	buffer_load_dwordx4 v[108:111], v1, s[4:7], s53 offen nt
	buffer_load_dwordx4 v[112:115], v1, s[4:7], s54 offen nt
	buffer_load_dwordx4 v[116:119], v1, s[4:7], s55 offen nt
	buffer_load_dwordx4 v[152:155], v1, s[8:11], s56 offen
	buffer_load_dwordx4 v[156:159], v1, s[8:11], s56 offen offset:1024
	buffer_load_dwordx4 v[160:163], v1, s[8:11], s56 offen offset:2048
	buffer_load_dwordx4 v[164:167], v1, s[8:11], s56 offen offset:3072
	s_waitcnt vmcnt(12)
	v_pk_mul_f32 v[24:25], v[16:17], s[32:33] op_sel_hi:[1,0]
	v_pk_mul_f32 v[26:27], v[18:19], s[32:33] op_sel_hi:[1,0]
	v_pk_mul_f32 v[28:29], v[20:21], s[40:41] op_sel_hi:[1,0]
	v_pk_mul_f32 v[30:31], v[22:23], s[40:41] op_sel_hi:[1,0]
	v_cmp_lt_i32_e64 s[60:61], 0, v120
	v_cmp_lt_i32_e64 s[62:63], 0, v121
	v_cmp_lt_i32_e64 s[64:65], 0, v122
	v_cmp_lt_i32_e64 s[66:67], 0, v123
	v_max_f32_e32 v24, v24, v28
	v_max_f32_e32 v25, v25, v29
	v_max_f32_e32 v26, v26, v30
	v_max_f32_e32 v27, v27, v31
	v_cndmask_b32_e64 v24, 0, v24, s[60:61]
	v_cndmask_b32_e64 v25, 0, v25, s[62:63]
	v_cndmask_b32_e64 v26, 0, v26, s[64:65]
	v_cndmask_b32_e64 v27, 0, v27, s[66:67]
	v_cvt_pkrtz_f16_f32 v32, v24, v25
	v_cvt_pkrtz_f16_f32 v33, v26, v27
	s_waitcnt lgkmcnt(0)
	v_pk_mul_f32 v[24:25], v[16:17], s[32:33] op_sel:[0,1] op_sel_hi:[1,1]
	v_pk_mul_f32 v[26:27], v[18:19], s[32:33] op_sel:[0,1] op_sel_hi:[1,1]
	v_pk_mul_f32 v[28:29], v[20:21], s[40:41] op_sel:[0,1] op_sel_hi:[1,1]
	v_pk_mul_f32 v[30:31], v[22:23], s[40:41] op_sel:[0,1] op_sel_hi:[1,1]
	v_mfma_f32_32x32x16_f16 v[40:55], v[184:187], v[200:203], v[40:55]
	v_cmp_lt_i32_e64 s[60:61], 0, v124
	v_cmp_lt_i32_e64 s[62:63], 0, v125
	v_cmp_lt_i32_e64 s[64:65], 0, v126
	v_cmp_lt_i32_e64 s[66:67], 0, v127
	v_max_f32_e32 v24, v24, v28
	v_max_f32_e32 v25, v25, v29
	v_max_f32_e32 v26, v26, v30
	v_max_f32_e32 v27, v27, v31
	v_cndmask_b32_e64 v24, 0, v24, s[60:61]
	v_cndmask_b32_e64 v25, 0, v25, s[62:63]
	v_cndmask_b32_e64 v26, 0, v26, s[64:65]
	v_cndmask_b32_e64 v27, 0, v27, s[66:67]
	v_mfma_f32_32x32x16_f16 v[56:71], v[184:187], v[204:207], v[56:71]
	v_cvt_pkrtz_f16_f32 v34, v24, v25
	v_cvt_pkrtz_f16_f32 v35, v26, v27
	ds_write2_b64 v5, v[32:33], v[34:35] offset0:0 offset1:66
	v_pk_mul_f32 v[24:25], v[16:17], s[34:35] op_sel_hi:[1,0]
	v_pk_mul_f32 v[26:27], v[18:19], s[34:35] op_sel_hi:[1,0]
	v_pk_mul_f32 v[28:29], v[20:21], s[42:43] op_sel_hi:[1,0]
	v_pk_mul_f32 v[30:31], v[22:23], s[42:43] op_sel_hi:[1,0]
	v_mfma_f32_32x32x16_f16 v[72:87], v[184:187], v[12:15], v[72:87]
	v_cmp_lt_i32_e64 s[60:61], 0, v128
	v_cmp_lt_i32_e64 s[62:63], 0, v129
	v_cmp_lt_i32_e64 s[64:65], 0, v130
	v_cmp_lt_i32_e64 s[66:67], 0, v131
	v_max_f32_e32 v24, v24, v28
	v_max_f32_e32 v25, v25, v29
	v_max_f32_e32 v26, v26, v30
	v_max_f32_e32 v27, v27, v31
	v_cndmask_b32_e64 v24, 0, v24, s[60:61]
	v_cndmask_b32_e64 v25, 0, v25, s[62:63]
	v_cndmask_b32_e64 v26, 0, v26, s[64:65]
	v_cndmask_b32_e64 v27, 0, v27, s[66:67]
	v_mfma_f32_32x32x16_f16 v[40:55], v[188:191], v[208:211], v[40:55]
	v_cvt_pkrtz_f16_f32 v32, v24, v25
	v_cvt_pkrtz_f16_f32 v33, v26, v27
	v_pk_mul_f32 v[24:25], v[16:17], s[34:35] op_sel:[0,1] op_sel_hi:[1,1]
	v_pk_mul_f32 v[26:27], v[18:19], s[34:35] op_sel:[0,1] op_sel_hi:[1,1]
	v_pk_mul_f32 v[28:29], v[20:21], s[42:43] op_sel:[0,1] op_sel_hi:[1,1]
	v_pk_mul_f32 v[30:31], v[22:23], s[42:43] op_sel:[0,1] op_sel_hi:[1,1]
	v_mfma_f32_32x32x16_f16 v[56:71], v[188:191], v[212:215], v[56:71]
	v_cmp_lt_i32_e64 s[60:61], 0, v132
	v_cmp_lt_i32_e64 s[62:63], 0, v133
	v_cmp_lt_i32_e64 s[64:65], 0, v134
	v_cmp_lt_i32_e64 s[66:67], 0, v135
	v_max_f32_e32 v24, v24, v28
	v_max_f32_e32 v25, v25, v29
	v_max_f32_e32 v26, v26, v30
	v_max_f32_e32 v27, v27, v31
	v_cndmask_b32_e64 v24, 0, v24, s[60:61]
	v_cndmask_b32_e64 v25, 0, v25, s[62:63]
	v_cndmask_b32_e64 v26, 0, v26, s[64:65]
	v_cndmask_b32_e64 v27, 0, v27, s[66:67]
	v_mfma_f32_32x32x16_f16 v[72:87], v[188:191], v[12:15], v[72:87]
	v_cvt_pkrtz_f16_f32 v34, v24, v25
	v_cvt_pkrtz_f16_f32 v35, v26, v27
	ds_write2_b64 v5, v[32:33], v[34:35] offset0:132 offset1:198
	v_pk_mul_f32 v[24:25], v[16:17], s[36:37] op_sel_hi:[1,0]
	v_pk_mul_f32 v[26:27], v[18:19], s[36:37] op_sel_hi:[1,0]
	v_pk_mul_f32 v[28:29], v[20:21], s[44:45] op_sel_hi:[1,0]
	v_pk_mul_f32 v[30:31], v[22:23], s[44:45] op_sel_hi:[1,0]
	v_mfma_f32_32x32x16_f16 v[40:55], v[192:195], v[216:219], v[40:55]
	v_cmp_lt_i32_e64 s[60:61], 0, v136
	v_cmp_lt_i32_e64 s[62:63], 0, v137
	v_cmp_lt_i32_e64 s[64:65], 0, v138
	v_cmp_lt_i32_e64 s[66:67], 0, v139
	v_max_f32_e32 v24, v24, v28
	v_max_f32_e32 v25, v25, v29
	v_max_f32_e32 v26, v26, v30
	v_max_f32_e32 v27, v27, v31
	v_cndmask_b32_e64 v24, 0, v24, s[60:61]
	v_cndmask_b32_e64 v25, 0, v25, s[62:63]
	v_cndmask_b32_e64 v26, 0, v26, s[64:65]
	v_cndmask_b32_e64 v27, 0, v27, s[66:67]
	v_mfma_f32_32x32x16_f16 v[56:71], v[192:195], v[220:223], v[56:71]
	v_cvt_pkrtz_f16_f32 v32, v24, v25
	v_cvt_pkrtz_f16_f32 v33, v26, v27
	v_pk_mul_f32 v[24:25], v[16:17], s[36:37] op_sel:[0,1] op_sel_hi:[1,1]
	v_pk_mul_f32 v[26:27], v[18:19], s[36:37] op_sel:[0,1] op_sel_hi:[1,1]
	v_pk_mul_f32 v[28:29], v[20:21], s[44:45] op_sel:[0,1] op_sel_hi:[1,1]
	v_pk_mul_f32 v[30:31], v[22:23], s[44:45] op_sel:[0,1] op_sel_hi:[1,1]
	v_mfma_f32_32x32x16_f16 v[72:87], v[192:195], v[12:15], v[72:87]
	v_cmp_lt_i32_e64 s[60:61], 0, v140
	v_cmp_lt_i32_e64 s[62:63], 0, v141
	v_cmp_lt_i32_e64 s[64:65], 0, v142
	v_cmp_lt_i32_e64 s[66:67], 0, v143
	v_max_f32_e32 v24, v24, v28
	v_max_f32_e32 v25, v25, v29
	v_max_f32_e32 v26, v26, v30
	v_max_f32_e32 v27, v27, v31
	v_cndmask_b32_e64 v24, 0, v24, s[60:61]
	v_cndmask_b32_e64 v25, 0, v25, s[62:63]
	v_cndmask_b32_e64 v26, 0, v26, s[64:65]
	v_cndmask_b32_e64 v27, 0, v27, s[66:67]
	v_mfma_f32_32x32x16_f16 v[40:55], v[196:199], v[224:227], v[40:55]
	v_cvt_pkrtz_f16_f32 v34, v24, v25
	v_cvt_pkrtz_f16_f32 v35, v26, v27
	ds_write2_b64 v6, v[32:33], v[34:35] offset0:0 offset1:66
	v_pk_mul_f32 v[24:25], v[16:17], s[38:39] op_sel_hi:[1,0]
	v_pk_mul_f32 v[26:27], v[18:19], s[38:39] op_sel_hi:[1,0]
	v_pk_mul_f32 v[28:29], v[20:21], s[46:47] op_sel_hi:[1,0]
	v_pk_mul_f32 v[30:31], v[22:23], s[46:47] op_sel_hi:[1,0]
	v_mfma_f32_32x32x16_f16 v[56:71], v[196:199], v[228:231], v[56:71]
	v_cmp_lt_i32_e64 s[60:61], 0, v144
	v_cmp_lt_i32_e64 s[62:63], 0, v145
	v_cmp_lt_i32_e64 s[64:65], 0, v146
	v_cmp_lt_i32_e64 s[66:67], 0, v147
	v_max_f32_e32 v24, v24, v28
	v_max_f32_e32 v25, v25, v29
	v_max_f32_e32 v26, v26, v30
	v_max_f32_e32 v27, v27, v31
	v_cndmask_b32_e64 v24, 0, v24, s[60:61]
	v_cndmask_b32_e64 v25, 0, v25, s[62:63]
	v_cndmask_b32_e64 v26, 0, v26, s[64:65]
	v_cndmask_b32_e64 v27, 0, v27, s[66:67]
	v_cvt_pkrtz_f16_f32 v32, v24, v25
	v_cvt_pkrtz_f16_f32 v33, v26, v27
	v_pk_mul_f32 v[24:25], v[16:17], s[38:39] op_sel:[0,1] op_sel_hi:[1,1]
	v_pk_mul_f32 v[26:27], v[18:19], s[38:39] op_sel:[0,1] op_sel_hi:[1,1]
	v_pk_mul_f32 v[28:29], v[20:21], s[46:47] op_sel:[0,1] op_sel_hi:[1,1]
	v_pk_mul_f32 v[30:31], v[22:23], s[46:47] op_sel:[0,1] op_sel_hi:[1,1]
	v_mfma_f32_32x32x16_f16 v[72:87], v[196:199], v[12:15], v[72:87]
	v_cmp_lt_i32_e64 s[60:61], 0, v148
	v_cmp_lt_i32_e64 s[62:63], 0, v149
	v_cmp_lt_i32_e64 s[64:65], 0, v150
	v_cmp_lt_i32_e64 s[66:67], 0, v151
	v_max_f32_e32 v24, v24, v28
	v_max_f32_e32 v25, v25, v29
	v_max_f32_e32 v26, v26, v30
	v_max_f32_e32 v27, v27, v31
	v_cndmask_b32_e64 v24, 0, v24, s[60:61]
	v_cndmask_b32_e64 v25, 0, v25, s[62:63]
	v_cndmask_b32_e64 v26, 0, v26, s[64:65]
	v_cndmask_b32_e64 v27, 0, v27, s[66:67]
	v_cvt_pkrtz_f16_f32 v34, v24, v25
	v_cvt_pkrtz_f16_f32 v35, v26, v27
	ds_write2_b64 v6, v[32:33], v[34:35] offset0:132 offset1:198
	ds_write_b128 v9, v[168:171] offset:32768
	ds_write_b128 v9, v[172:175] offset:33792
	ds_write_b128 v9, v[176:179] offset:34816
	ds_write_b128 v9, v[180:183] offset:35840
	s_add_u32 s3, s19, 6
	s_and_b32 s3, s3, 7
	s_lshl_b32 s3, s3, 10
	v_add_u32_e32 v11, s3, v10
	ds_read_b128 v[16:19], v11
	ds_read_b128 v[20:23], v11 offset:8192
	s_waitcnt lgkmcnt(0)
	s_barrier
	ds_read_b128 v[184:187], v7 offset:33792
	ds_read_b128 v[200:203], v8 offset:32768
	ds_read_b128 v[204:207], v8 offset:33792
	ds_read_b128 v[188:191], v7 offset:33824
	ds_read_b128 v[208:211], v8 offset:34816
	ds_read_b128 v[212:215], v8 offset:35840
	ds_read_b128 v[192:195], v7 offset:33856
	ds_read_b128 v[216:219], v8 offset:36864
	ds_read_b128 v[220:223], v8 offset:37888
	ds_read_b128 v[196:199], v7 offset:33888
	ds_read_b128 v[224:227], v8 offset:38912
	ds_read_b128 v[228:231], v8 offset:39936
	s_add_u32 s3, s19, 7
	s_and_b32 s3, s3, 7
	s_lshl_b32 s57, s3, 10
	s_add_u32 s48, s57, s22
	s_add_u32 s49, s48, 0x2000
	s_add_u32 s50, s48, 0x4000
	s_add_u32 s51, s48, 0x6000
	s_add_u32 s52, s48, 0x8000
	s_add_u32 s53, s48, 0xa000
	s_add_u32 s54, s48, 0xc000
	s_add_u32 s55, s48, 0xe000
	s_lshl_b32 s56, s3, 15
	s_add_u32 s56, s56, s23
	buffer_load_dwordx4 v[120:123], v1, s[4:7], s48 offen nt
	buffer_load_dwordx4 v[124:127], v1, s[4:7], s49 offen nt
	buffer_load_dwordx4 v[128:131], v1, s[4:7], s50 offen nt
	buffer_load_dwordx4 v[132:135], v1, s[4:7], s51 offen nt
	buffer_load_dwordx4 v[136:139], v1, s[4:7], s52 offen nt
	buffer_load_dwordx4 v[140:143], v1, s[4:7], s53 offen nt
	buffer_load_dwordx4 v[144:147], v1, s[4:7], s54 offen nt
	buffer_load_dwordx4 v[148:151], v1, s[4:7], s55 offen nt
	buffer_load_dwordx4 v[168:171], v1, s[8:11], s56 offen
	buffer_load_dwordx4 v[172:175], v1, s[8:11], s56 offen offset:1024
	buffer_load_dwordx4 v[176:179], v1, s[8:11], s56 offen offset:2048
	buffer_load_dwordx4 v[180:183], v1, s[8:11], s56 offen offset:3072
	s_waitcnt vmcnt(12)
	v_pk_mul_f32 v[24:25], v[16:17], s[32:33] op_sel_hi:[1,0]
	v_pk_mul_f32 v[26:27], v[18:19], s[32:33] op_sel_hi:[1,0]
	v_pk_mul_f32 v[28:29], v[20:21], s[40:41] op_sel_hi:[1,0]
	v_pk_mul_f32 v[30:31], v[22:23], s[40:41] op_sel_hi:[1,0]
	v_cmp_lt_i32_e64 s[60:61], 0, v88
	v_cmp_lt_i32_e64 s[62:63], 0, v89
	v_cmp_lt_i32_e64 s[64:65], 0, v90
	v_cmp_lt_i32_e64 s[66:67], 0, v91
	v_max_f32_e32 v24, v24, v28
	v_max_f32_e32 v25, v25, v29
	v_max_f32_e32 v26, v26, v30
	v_max_f32_e32 v27, v27, v31
	v_cndmask_b32_e64 v24, 0, v24, s[60:61]
	v_cndmask_b32_e64 v25, 0, v25, s[62:63]
	v_cndmask_b32_e64 v26, 0, v26, s[64:65]
	v_cndmask_b32_e64 v27, 0, v27, s[66:67]
	v_cvt_pkrtz_f16_f32 v32, v24, v25
	v_cvt_pkrtz_f16_f32 v33, v26, v27
	s_waitcnt lgkmcnt(0)
	v_pk_mul_f32 v[24:25], v[16:17], s[32:33] op_sel:[0,1] op_sel_hi:[1,1]
	v_pk_mul_f32 v[26:27], v[18:19], s[32:33] op_sel:[0,1] op_sel_hi:[1,1]
	v_pk_mul_f32 v[28:29], v[20:21], s[40:41] op_sel:[0,1] op_sel_hi:[1,1]
	v_pk_mul_f32 v[30:31], v[22:23], s[40:41] op_sel:[0,1] op_sel_hi:[1,1]
	v_mfma_f32_32x32x16_f16 v[40:55], v[184:187], v[200:203], v[40:55]
	v_cmp_lt_i32_e64 s[60:61], 0, v92
	v_cmp_lt_i32_e64 s[62:63], 0, v93
	v_cmp_lt_i32_e64 s[64:65], 0, v94
	v_cmp_lt_i32_e64 s[66:67], 0, v95
	v_max_f32_e32 v24, v24, v28
	v_max_f32_e32 v25, v25, v29
	v_max_f32_e32 v26, v26, v30
	v_max_f32_e32 v27, v27, v31
	v_cndmask_b32_e64 v24, 0, v24, s[60:61]
	v_cndmask_b32_e64 v25, 0, v25, s[62:63]
	v_cndmask_b32_e64 v26, 0, v26, s[64:65]
	v_cndmask_b32_e64 v27, 0, v27, s[66:67]
	v_mfma_f32_32x32x16_f16 v[56:71], v[184:187], v[204:207], v[56:71]
	v_cvt_pkrtz_f16_f32 v34, v24, v25
	v_cvt_pkrtz_f16_f32 v35, v26, v27
	ds_write2_b64 v3, v[32:33], v[34:35] offset0:0 offset1:66
	v_pk_mul_f32 v[24:25], v[16:17], s[34:35] op_sel_hi:[1,0]
	v_pk_mul_f32 v[26:27], v[18:19], s[34:35] op_sel_hi:[1,0]
	v_pk_mul_f32 v[28:29], v[20:21], s[42:43] op_sel_hi:[1,0]
	v_pk_mul_f32 v[30:31], v[22:23], s[42:43] op_sel_hi:[1,0]
	v_mfma_f32_32x32x16_f16 v[72:87], v[184:187], v[12:15], v[72:87]
	v_cmp_lt_i32_e64 s[60:61], 0, v96
	v_cmp_lt_i32_e64 s[62:63], 0, v97
	v_cmp_lt_i32_e64 s[64:65], 0, v98
	v_cmp_lt_i32_e64 s[66:67], 0, v99
	v_max_f32_e32 v24, v24, v28
	v_max_f32_e32 v25, v25, v29
	v_max_f32_e32 v26, v26, v30
	v_max_f32_e32 v27, v27, v31
	v_cndmask_b32_e64 v24, 0, v24, s[60:61]
	v_cndmask_b32_e64 v25, 0, v25, s[62:63]
	v_cndmask_b32_e64 v26, 0, v26, s[64:65]
	v_cndmask_b32_e64 v27, 0, v27, s[66:67]
	v_mfma_f32_32x32x16_f16 v[40:55], v[188:191], v[208:211], v[40:55]
	v_cvt_pkrtz_f16_f32 v32, v24, v25
	v_cvt_pkrtz_f16_f32 v33, v26, v27
	v_pk_mul_f32 v[24:25], v[16:17], s[34:35] op_sel:[0,1] op_sel_hi:[1,1]
	v_pk_mul_f32 v[26:27], v[18:19], s[34:35] op_sel:[0,1] op_sel_hi:[1,1]
	v_pk_mul_f32 v[28:29], v[20:21], s[42:43] op_sel:[0,1] op_sel_hi:[1,1]
	v_pk_mul_f32 v[30:31], v[22:23], s[42:43] op_sel:[0,1] op_sel_hi:[1,1]
	v_mfma_f32_32x32x16_f16 v[56:71], v[188:191], v[212:215], v[56:71]
	v_cmp_lt_i32_e64 s[60:61], 0, v100
	v_cmp_lt_i32_e64 s[62:63], 0, v101
	v_cmp_lt_i32_e64 s[64:65], 0, v102
	v_cmp_lt_i32_e64 s[66:67], 0, v103
	v_max_f32_e32 v24, v24, v28
	v_max_f32_e32 v25, v25, v29
	v_max_f32_e32 v26, v26, v30
	v_max_f32_e32 v27, v27, v31
	v_cndmask_b32_e64 v24, 0, v24, s[60:61]
	v_cndmask_b32_e64 v25, 0, v25, s[62:63]
	v_cndmask_b32_e64 v26, 0, v26, s[64:65]
	v_cndmask_b32_e64 v27, 0, v27, s[66:67]
	v_mfma_f32_32x32x16_f16 v[72:87], v[188:191], v[12:15], v[72:87]
	v_cvt_pkrtz_f16_f32 v34, v24, v25
	v_cvt_pkrtz_f16_f32 v35, v26, v27
	ds_write2_b64 v3, v[32:33], v[34:35] offset0:132 offset1:198
	v_pk_mul_f32 v[24:25], v[16:17], s[36:37] op_sel_hi:[1,0]
	v_pk_mul_f32 v[26:27], v[18:19], s[36:37] op_sel_hi:[1,0]
	v_pk_mul_f32 v[28:29], v[20:21], s[44:45] op_sel_hi:[1,0]
	v_pk_mul_f32 v[30:31], v[22:23], s[44:45] op_sel_hi:[1,0]
	v_mfma_f32_32x32x16_f16 v[40:55], v[192:195], v[216:219], v[40:55]
	v_cmp_lt_i32_e64 s[60:61], 0, v104
	v_cmp_lt_i32_e64 s[62:63], 0, v105
	v_cmp_lt_i32_e64 s[64:65], 0, v106
	v_cmp_lt_i32_e64 s[66:67], 0, v107
	v_max_f32_e32 v24, v24, v28
	v_max_f32_e32 v25, v25, v29
	v_max_f32_e32 v26, v26, v30
	v_max_f32_e32 v27, v27, v31
	v_cndmask_b32_e64 v24, 0, v24, s[60:61]
	v_cndmask_b32_e64 v25, 0, v25, s[62:63]
	v_cndmask_b32_e64 v26, 0, v26, s[64:65]
	v_cndmask_b32_e64 v27, 0, v27, s[66:67]
	v_mfma_f32_32x32x16_f16 v[56:71], v[192:195], v[220:223], v[56:71]
	v_cvt_pkrtz_f16_f32 v32, v24, v25
	v_cvt_pkrtz_f16_f32 v33, v26, v27
	v_pk_mul_f32 v[24:25], v[16:17], s[36:37] op_sel:[0,1] op_sel_hi:[1,1]
	v_pk_mul_f32 v[26:27], v[18:19], s[36:37] op_sel:[0,1] op_sel_hi:[1,1]
	v_pk_mul_f32 v[28:29], v[20:21], s[44:45] op_sel:[0,1] op_sel_hi:[1,1]
	v_pk_mul_f32 v[30:31], v[22:23], s[44:45] op_sel:[0,1] op_sel_hi:[1,1]
	v_mfma_f32_32x32x16_f16 v[72:87], v[192:195], v[12:15], v[72:87]
	v_cmp_lt_i32_e64 s[60:61], 0, v108
	v_cmp_lt_i32_e64 s[62:63], 0, v109
	v_cmp_lt_i32_e64 s[64:65], 0, v110
	v_cmp_lt_i32_e64 s[66:67], 0, v111
	v_max_f32_e32 v24, v24, v28
	v_max_f32_e32 v25, v25, v29
	v_max_f32_e32 v26, v26, v30
	v_max_f32_e32 v27, v27, v31
	v_cndmask_b32_e64 v24, 0, v24, s[60:61]
	v_cndmask_b32_e64 v25, 0, v25, s[62:63]
	v_cndmask_b32_e64 v26, 0, v26, s[64:65]
	v_cndmask_b32_e64 v27, 0, v27, s[66:67]
	v_mfma_f32_32x32x16_f16 v[40:55], v[196:199], v[224:227], v[40:55]
	v_cvt_pkrtz_f16_f32 v34, v24, v25
	v_cvt_pkrtz_f16_f32 v35, v26, v27
	ds_write2_b64 v4, v[32:33], v[34:35] offset0:0 offset1:66
	v_pk_mul_f32 v[24:25], v[16:17], s[38:39] op_sel_hi:[1,0]
	v_pk_mul_f32 v[26:27], v[18:19], s[38:39] op_sel_hi:[1,0]
	v_pk_mul_f32 v[28:29], v[20:21], s[46:47] op_sel_hi:[1,0]
	v_pk_mul_f32 v[30:31], v[22:23], s[46:47] op_sel_hi:[1,0]
	v_mfma_f32_32x32x16_f16 v[56:71], v[196:199], v[228:231], v[56:71]
	v_cmp_lt_i32_e64 s[60:61], 0, v112
	v_cmp_lt_i32_e64 s[62:63], 0, v113
	v_cmp_lt_i32_e64 s[64:65], 0, v114
	v_cmp_lt_i32_e64 s[66:67], 0, v115
	v_max_f32_e32 v24, v24, v28
	v_max_f32_e32 v25, v25, v29
	v_max_f32_e32 v26, v26, v30
	v_max_f32_e32 v27, v27, v31
	v_cndmask_b32_e64 v24, 0, v24, s[60:61]
	v_cndmask_b32_e64 v25, 0, v25, s[62:63]
	v_cndmask_b32_e64 v26, 0, v26, s[64:65]
	v_cndmask_b32_e64 v27, 0, v27, s[66:67]
	v_cvt_pkrtz_f16_f32 v32, v24, v25
	v_cvt_pkrtz_f16_f32 v33, v26, v27
	v_pk_mul_f32 v[24:25], v[16:17], s[38:39] op_sel:[0,1] op_sel_hi:[1,1]
	v_pk_mul_f32 v[26:27], v[18:19], s[38:39] op_sel:[0,1] op_sel_hi:[1,1]
	v_pk_mul_f32 v[28:29], v[20:21], s[46:47] op_sel:[0,1] op_sel_hi:[1,1]
	v_pk_mul_f32 v[30:31], v[22:23], s[46:47] op_sel:[0,1] op_sel_hi:[1,1]
	v_mfma_f32_32x32x16_f16 v[72:87], v[196:199], v[12:15], v[72:87]
	v_cmp_lt_i32_e64 s[60:61], 0, v116
	v_cmp_lt_i32_e64 s[62:63], 0, v117
	v_cmp_lt_i32_e64 s[64:65], 0, v118
	v_cmp_lt_i32_e64 s[66:67], 0, v119
	v_max_f32_e32 v24, v24, v28
	v_max_f32_e32 v25, v25, v29
	v_max_f32_e32 v26, v26, v30
	v_max_f32_e32 v27, v27, v31
	v_cndmask_b32_e64 v24, 0, v24, s[60:61]
	v_cndmask_b32_e64 v25, 0, v25, s[62:63]
	v_cndmask_b32_e64 v26, 0, v26, s[64:65]
	v_cndmask_b32_e64 v27, 0, v27, s[66:67]
	v_cvt_pkrtz_f16_f32 v34, v24, v25
	v_cvt_pkrtz_f16_f32 v35, v26, v27
	ds_write2_b64 v4, v[32:33], v[34:35] offset0:132 offset1:198
	ds_write_b128 v9, v[152:155] offset:0
	ds_write_b128 v9, v[156:159] offset:1024
	ds_write_b128 v9, v[160:163] offset:2048
	ds_write_b128 v9, v[164:167] offset:3072
	s_add_u32 s3, s19, 7
	s_and_b32 s3, s3, 7
	s_lshl_b32 s3, s3, 10
	v_add_u32_e32 v11, s3, v10
	ds_read_b128 v[16:19], v11
	ds_read_b128 v[20:23], v11 offset:8192
	s_waitcnt lgkmcnt(0)
	s_barrier
	ds_read_b128 v[184:187], v7 offset:0
	ds_read_b128 v[200:203], v8 offset:0
	ds_read_b128 v[204:207], v8 offset:1024
	ds_read_b128 v[188:191], v7 offset:32
	ds_read_b128 v[208:211], v8 offset:2048
	ds_read_b128 v[212:215], v8 offset:3072
	ds_read_b128 v[192:195], v7 offset:64
	ds_read_b128 v[216:219], v8 offset:4096
	ds_read_b128 v[220:223], v8 offset:5120
	ds_read_b128 v[196:199], v7 offset:96
	ds_read_b128 v[224:227], v8 offset:6144
	ds_read_b128 v[228:231], v8 offset:7168
	s_waitcnt vmcnt(0)
	v_pk_mul_f32 v[24:25], v[16:17], s[32:33] op_sel_hi:[1,0]
	v_pk_mul_f32 v[26:27], v[18:19], s[32:33] op_sel_hi:[1,0]
	v_pk_mul_f32 v[28:29], v[20:21], s[40:41] op_sel_hi:[1,0]
	v_pk_mul_f32 v[30:31], v[22:23], s[40:41] op_sel_hi:[1,0]
	v_cmp_lt_i32_e64 s[60:61], 0, v120
	v_cmp_lt_i32_e64 s[62:63], 0, v121
	v_cmp_lt_i32_e64 s[64:65], 0, v122
	v_cmp_lt_i32_e64 s[66:67], 0, v123
	v_max_f32_e32 v24, v24, v28
	v_max_f32_e32 v25, v25, v29
	v_max_f32_e32 v26, v26, v30
	v_max_f32_e32 v27, v27, v31
	v_cndmask_b32_e64 v24, 0, v24, s[60:61]
	v_cndmask_b32_e64 v25, 0, v25, s[62:63]
	v_cndmask_b32_e64 v26, 0, v26, s[64:65]
	v_cndmask_b32_e64 v27, 0, v27, s[66:67]
	v_cvt_pkrtz_f16_f32 v32, v24, v25
	v_cvt_pkrtz_f16_f32 v33, v26, v27
	s_waitcnt lgkmcnt(0)
	v_pk_mul_f32 v[24:25], v[16:17], s[32:33] op_sel:[0,1] op_sel_hi:[1,1]
	v_pk_mul_f32 v[26:27], v[18:19], s[32:33] op_sel:[0,1] op_sel_hi:[1,1]
	v_pk_mul_f32 v[28:29], v[20:21], s[40:41] op_sel:[0,1] op_sel_hi:[1,1]
	v_pk_mul_f32 v[30:31], v[22:23], s[40:41] op_sel:[0,1] op_sel_hi:[1,1]
	v_mfma_f32_32x32x16_f16 v[40:55], v[184:187], v[200:203], v[40:55]
	v_cmp_lt_i32_e64 s[60:61], 0, v124
	v_cmp_lt_i32_e64 s[62:63], 0, v125
	v_cmp_lt_i32_e64 s[64:65], 0, v126
	v_cmp_lt_i32_e64 s[66:67], 0, v127
	v_max_f32_e32 v24, v24, v28
	v_max_f32_e32 v25, v25, v29
	v_max_f32_e32 v26, v26, v30
	v_max_f32_e32 v27, v27, v31
	v_cndmask_b32_e64 v24, 0, v24, s[60:61]
	v_cndmask_b32_e64 v25, 0, v25, s[62:63]
	v_cndmask_b32_e64 v26, 0, v26, s[64:65]
	v_cndmask_b32_e64 v27, 0, v27, s[66:67]
	v_mfma_f32_32x32x16_f16 v[56:71], v[184:187], v[204:207], v[56:71]
	v_cvt_pkrtz_f16_f32 v34, v24, v25
	v_cvt_pkrtz_f16_f32 v35, v26, v27
	ds_write2_b64 v5, v[32:33], v[34:35] offset0:0 offset1:66
	v_pk_mul_f32 v[24:25], v[16:17], s[34:35] op_sel_hi:[1,0]
	v_pk_mul_f32 v[26:27], v[18:19], s[34:35] op_sel_hi:[1,0]
	v_pk_mul_f32 v[28:29], v[20:21], s[42:43] op_sel_hi:[1,0]
	v_pk_mul_f32 v[30:31], v[22:23], s[42:43] op_sel_hi:[1,0]
	v_mfma_f32_32x32x16_f16 v[72:87], v[184:187], v[12:15], v[72:87]
	v_cmp_lt_i32_e64 s[60:61], 0, v128
	v_cmp_lt_i32_e64 s[62:63], 0, v129
	v_cmp_lt_i32_e64 s[64:65], 0, v130
	v_cmp_lt_i32_e64 s[66:67], 0, v131
	v_max_f32_e32 v24, v24, v28
	v_max_f32_e32 v25, v25, v29
	v_max_f32_e32 v26, v26, v30
	v_max_f32_e32 v27, v27, v31
	v_cndmask_b32_e64 v24, 0, v24, s[60:61]
	v_cndmask_b32_e64 v25, 0, v25, s[62:63]
	v_cndmask_b32_e64 v26, 0, v26, s[64:65]
	v_cndmask_b32_e64 v27, 0, v27, s[66:67]
	v_mfma_f32_32x32x16_f16 v[40:55], v[188:191], v[208:211], v[40:55]
	v_cvt_pkrtz_f16_f32 v32, v24, v25
	v_cvt_pkrtz_f16_f32 v33, v26, v27
	v_pk_mul_f32 v[24:25], v[16:17], s[34:35] op_sel:[0,1] op_sel_hi:[1,1]
	v_pk_mul_f32 v[26:27], v[18:19], s[34:35] op_sel:[0,1] op_sel_hi:[1,1]
	v_pk_mul_f32 v[28:29], v[20:21], s[42:43] op_sel:[0,1] op_sel_hi:[1,1]
	v_pk_mul_f32 v[30:31], v[22:23], s[42:43] op_sel:[0,1] op_sel_hi:[1,1]
	v_mfma_f32_32x32x16_f16 v[56:71], v[188:191], v[212:215], v[56:71]
	v_cmp_lt_i32_e64 s[60:61], 0, v132
	v_cmp_lt_i32_e64 s[62:63], 0, v133
	v_cmp_lt_i32_e64 s[64:65], 0, v134
	v_cmp_lt_i32_e64 s[66:67], 0, v135
	v_max_f32_e32 v24, v24, v28
	v_max_f32_e32 v25, v25, v29
	v_max_f32_e32 v26, v26, v30
	v_max_f32_e32 v27, v27, v31
	v_cndmask_b32_e64 v24, 0, v24, s[60:61]
	v_cndmask_b32_e64 v25, 0, v25, s[62:63]
	v_cndmask_b32_e64 v26, 0, v26, s[64:65]
	v_cndmask_b32_e64 v27, 0, v27, s[66:67]
	v_mfma_f32_32x32x16_f16 v[72:87], v[188:191], v[12:15], v[72:87]
	v_cvt_pkrtz_f16_f32 v34, v24, v25
	v_cvt_pkrtz_f16_f32 v35, v26, v27
	ds_write2_b64 v5, v[32:33], v[34:35] offset0:132 offset1:198
	v_pk_mul_f32 v[24:25], v[16:17], s[36:37] op_sel_hi:[1,0]
	v_pk_mul_f32 v[26:27], v[18:19], s[36:37] op_sel_hi:[1,0]
	v_pk_mul_f32 v[28:29], v[20:21], s[44:45] op_sel_hi:[1,0]
	v_pk_mul_f32 v[30:31], v[22:23], s[44:45] op_sel_hi:[1,0]
	v_mfma_f32_32x32x16_f16 v[40:55], v[192:195], v[216:219], v[40:55]
	v_cmp_lt_i32_e64 s[60:61], 0, v136
	v_cmp_lt_i32_e64 s[62:63], 0, v137
	v_cmp_lt_i32_e64 s[64:65], 0, v138
	v_cmp_lt_i32_e64 s[66:67], 0, v139
	v_max_f32_e32 v24, v24, v28
	v_max_f32_e32 v25, v25, v29
	v_max_f32_e32 v26, v26, v30
	v_max_f32_e32 v27, v27, v31
	v_cndmask_b32_e64 v24, 0, v24, s[60:61]
	v_cndmask_b32_e64 v25, 0, v25, s[62:63]
	v_cndmask_b32_e64 v26, 0, v26, s[64:65]
	v_cndmask_b32_e64 v27, 0, v27, s[66:67]
	v_mfma_f32_32x32x16_f16 v[56:71], v[192:195], v[220:223], v[56:71]
	v_cvt_pkrtz_f16_f32 v32, v24, v25
	v_cvt_pkrtz_f16_f32 v33, v26, v27
	v_pk_mul_f32 v[24:25], v[16:17], s[36:37] op_sel:[0,1] op_sel_hi:[1,1]
	v_pk_mul_f32 v[26:27], v[18:19], s[36:37] op_sel:[0,1] op_sel_hi:[1,1]
	v_pk_mul_f32 v[28:29], v[20:21], s[44:45] op_sel:[0,1] op_sel_hi:[1,1]
	v_pk_mul_f32 v[30:31], v[22:23], s[44:45] op_sel:[0,1] op_sel_hi:[1,1]
	v_mfma_f32_32x32x16_f16 v[72:87], v[192:195], v[12:15], v[72:87]
	v_cmp_lt_i32_e64 s[60:61], 0, v140
	v_cmp_lt_i32_e64 s[62:63], 0, v141
	v_cmp_lt_i32_e64 s[64:65], 0, v142
	v_cmp_lt_i32_e64 s[66:67], 0, v143
	v_max_f32_e32 v24, v24, v28
	v_max_f32_e32 v25, v25, v29
	v_max_f32_e32 v26, v26, v30
	v_max_f32_e32 v27, v27, v31
	v_cndmask_b32_e64 v24, 0, v24, s[60:61]
	v_cndmask_b32_e64 v25, 0, v25, s[62:63]
	v_cndmask_b32_e64 v26, 0, v26, s[64:65]
	v_cndmask_b32_e64 v27, 0, v27, s[66:67]
	v_mfma_f32_32x32x16_f16 v[40:55], v[196:199], v[224:227], v[40:55]
	v_cvt_pkrtz_f16_f32 v34, v24, v25
	v_cvt_pkrtz_f16_f32 v35, v26, v27
	ds_write2_b64 v6, v[32:33], v[34:35] offset0:0 offset1:66
	v_pk_mul_f32 v[24:25], v[16:17], s[38:39] op_sel_hi:[1,0]
	v_pk_mul_f32 v[26:27], v[18:19], s[38:39] op_sel_hi:[1,0]
	v_pk_mul_f32 v[28:29], v[20:21], s[46:47] op_sel_hi:[1,0]
	v_pk_mul_f32 v[30:31], v[22:23], s[46:47] op_sel_hi:[1,0]
	v_mfma_f32_32x32x16_f16 v[56:71], v[196:199], v[228:231], v[56:71]
	v_cmp_lt_i32_e64 s[60:61], 0, v144
	v_cmp_lt_i32_e64 s[62:63], 0, v145
	v_cmp_lt_i32_e64 s[64:65], 0, v146
	v_cmp_lt_i32_e64 s[66:67], 0, v147
	v_max_f32_e32 v24, v24, v28
	v_max_f32_e32 v25, v25, v29
	v_max_f32_e32 v26, v26, v30
	v_max_f32_e32 v27, v27, v31
	v_cndmask_b32_e64 v24, 0, v24, s[60:61]
	v_cndmask_b32_e64 v25, 0, v25, s[62:63]
	v_cndmask_b32_e64 v26, 0, v26, s[64:65]
	v_cndmask_b32_e64 v27, 0, v27, s[66:67]
	v_cvt_pkrtz_f16_f32 v32, v24, v25
	v_cvt_pkrtz_f16_f32 v33, v26, v27
	v_pk_mul_f32 v[24:25], v[16:17], s[38:39] op_sel:[0,1] op_sel_hi:[1,1]
	v_pk_mul_f32 v[26:27], v[18:19], s[38:39] op_sel:[0,1] op_sel_hi:[1,1]
	v_pk_mul_f32 v[28:29], v[20:21], s[46:47] op_sel:[0,1] op_sel_hi:[1,1]
	v_pk_mul_f32 v[30:31], v[22:23], s[46:47] op_sel:[0,1] op_sel_hi:[1,1]
	v_mfma_f32_32x32x16_f16 v[72:87], v[196:199], v[12:15], v[72:87]
	v_cmp_lt_i32_e64 s[60:61], 0, v148
	v_cmp_lt_i32_e64 s[62:63], 0, v149
	v_cmp_lt_i32_e64 s[64:65], 0, v150
	v_cmp_lt_i32_e64 s[66:67], 0, v151
	v_max_f32_e32 v24, v24, v28
	v_max_f32_e32 v25, v25, v29
	v_max_f32_e32 v26, v26, v30
	v_max_f32_e32 v27, v27, v31
	v_cndmask_b32_e64 v24, 0, v24, s[60:61]
	v_cndmask_b32_e64 v25, 0, v25, s[62:63]
	v_cndmask_b32_e64 v26, 0, v26, s[64:65]
	v_cndmask_b32_e64 v27, 0, v27, s[66:67]
	v_cvt_pkrtz_f16_f32 v34, v24, v25
	v_cvt_pkrtz_f16_f32 v35, v26, v27
	ds_write2_b64 v6, v[32:33], v[34:35] offset0:132 offset1:198
	ds_write_b128 v9, v[168:171] offset:32768
	ds_write_b128 v9, v[172:175] offset:33792
	ds_write_b128 v9, v[176:179] offset:34816
	ds_write_b128 v9, v[180:183] offset:35840
	s_waitcnt lgkmcnt(0)
	s_barrier
	ds_read_b128 v[184:187], v7 offset:33792
	ds_read_b128 v[200:203], v8 offset:32768
	ds_read_b128 v[204:207], v8 offset:33792
	ds_read_b128 v[188:191], v7 offset:33824
	ds_read_b128 v[208:211], v8 offset:34816
	ds_read_b128 v[212:215], v8 offset:35840
	ds_read_b128 v[192:195], v7 offset:33856
	ds_read_b128 v[216:219], v8 offset:36864
	ds_read_b128 v[220:223], v8 offset:37888
	ds_read_b128 v[196:199], v7 offset:33888
	ds_read_b128 v[224:227], v8 offset:38912
	ds_read_b128 v[228:231], v8 offset:39936
	s_waitcnt lgkmcnt(0)
	v_mfma_f32_32x32x16_f16 v[40:55], v[184:187], v[200:203], v[40:55]
	v_mfma_f32_32x32x16_f16 v[56:71], v[184:187], v[204:207], v[56:71]
	v_mfma_f32_32x32x16_f16 v[72:87], v[184:187], v[12:15], v[72:87]
	v_mfma_f32_32x32x16_f16 v[40:55], v[188:191], v[208:211], v[40:55]
	v_mfma_f32_32x32x16_f16 v[56:71], v[188:191], v[212:215], v[56:71]
	v_mfma_f32_32x32x16_f16 v[72:87], v[188:191], v[12:15], v[72:87]
	v_mfma_f32_32x32x16_f16 v[40:55], v[192:195], v[216:219], v[40:55]
	v_mfma_f32_32x32x16_f16 v[56:71], v[192:195], v[220:223], v[56:71]
	v_mfma_f32_32x32x16_f16 v[72:87], v[192:195], v[12:15], v[72:87]
	v_mfma_f32_32x32x16_f16 v[40:55], v[196:199], v[224:227], v[40:55]
	v_mfma_f32_32x32x16_f16 v[56:71], v[196:199], v[228:231], v[56:71]
	v_mfma_f32_32x32x16_f16 v[72:87], v[196:199], v[12:15], v[72:87]
	s_nop 15
	s_barrier
	s_mul_i32 s3, s20, 0xc000
	s_mul_i32 s57, s21, 0xc00
	s_add_u32 s3, s3, s57
	v_add_u32_e32 v36, s3, v1
	ds_write_b128 v36, v[40:43] offset:0
	ds_write_b128 v36, v[56:59] offset:1024
	ds_write_b128 v36, v[72:75] offset:2048
	ds_write_b128 v36, v[44:47] offset:12288
	ds_write_b128 v36, v[60:63] offset:13312
	ds_write_b128 v36, v[76:79] offset:14336
	ds_write_b128 v36, v[48:51] offset:24576
	ds_write_b128 v36, v[64:67] offset:25600
	ds_write_b128 v36, v[80:83] offset:26624
	ds_write_b128 v36, v[52:55] offset:36864
	ds_write_b128 v36, v[68:71] offset:37888
	ds_write_b128 v36, v[84:87] offset:38912
	s_waitcnt lgkmcnt(0)
	s_barrier
	s_mul_i32 s3, s16, 0x3000
	v_add_u32_e32 v36, s3, v1
	ds_read_b128 v[40:43], v36 offset:0
	ds_read_b128 v[44:47], v36 offset:1024
	ds_read_b128 v[48:51], v36 offset:2048
	ds_read_b128 v[52:55], v36 offset:3072
	ds_read_b128 v[56:59], v36 offset:4096
	ds_read_b128 v[60:63], v36 offset:5120
	ds_read_b128 v[64:67], v36 offset:6144
	ds_read_b128 v[68:71], v36 offset:7168
	ds_read_b128 v[72:75], v36 offset:8192
	ds_read_b128 v[76:79], v36 offset:9216
	ds_read_b128 v[80:83], v36 offset:10240
	ds_read_b128 v[84:87], v36 offset:11264
	s_waitcnt lgkmcnt(0)
	v_add_f32_e32 v40, v40, v52
	v_add_f32_e32 v41, v41, v53
	v_add_f32_e32 v42, v42, v54
	v_add_f32_e32 v43, v43, v55
	v_add_f32_e32 v44, v44, v56
	v_add_f32_e32 v45, v45, v57
	v_add_f32_e32 v46, v46, v58
	v_add_f32_e32 v47, v47, v59
	v_add_f32_e32 v48, v48, v60
	v_add_f32_e32 v49, v49, v61
	v_add_f32_e32 v50, v50, v62
	v_add_f32_e32 v51, v51, v63
	v_add_f32_e32 v40, v40, v64
	v_add_f32_e32 v41, v41, v65
	v_add_f32_e32 v42, v42, v66
	v_add_f32_e32 v43, v43, v67
	v_add_f32_e32 v44, v44, v68
	v_add_f32_e32 v45, v45, v69
	v_add_f32_e32 v46, v46, v70
	v_add_f32_e32 v47, v47, v71
	v_add_f32_e32 v48, v48, v72
	v_add_f32_e32 v49, v49, v73
	v_add_f32_e32 v50, v50, v74
	v_add_f32_e32 v51, v51, v75
	v_add_f32_e32 v40, v40, v76
	v_add_f32_e32 v41, v41, v77
	v_add_f32_e32 v42, v42, v78
	v_add_f32_e32 v43, v43, v79
	v_add_f32_e32 v44, v44, v80
	v_add_f32_e32 v45, v45, v81
	v_add_f32_e32 v46, v46, v82
	v_add_f32_e32 v47, v47, v83
	v_add_f32_e32 v48, v48, v84
	v_add_f32_e32 v49, v49, v85
	v_add_f32_e32 v50, v50, v86
	v_add_f32_e32 v51, v51, v87
	v_cmp_eq_f32_e64 s[60:61], 0, v48
	v_cmp_eq_f32_e64 s[62:63], 0, v49
	v_cmp_eq_f32_e64 s[64:65], 0, v50
	v_cmp_eq_f32_e64 s[66:67], 0, v51
	s_nop 3
	s_or_b64 s[60:61], s[60:61], s[62:63]
	s_or_b64 s[64:65], s[64:65], s[66:67]
	s_or_b64 s[60:61], s[60:61], s[64:65]
	s_cmp_eq_u64 s[60:61], 0
	s_cbranch_scc1 .Lgm_no_fallback
	v_and_b32_e32 v101, 31, v2
	v_lshlrev_b32_e32 v101, 4, v101
	v_mov_b32_e32 v88, 0
	v_mov_b32_e32 v89, 0
	s_mov_b32 s3, 0

	.amdhsa_kernel _Z8gat_mainPKiPKDF16_PKfS4_Pf
		.amdhsa_group_segment_fixed_size 149536
		.amdhsa_private_segment_fixed_size 0
		.amdhsa_kernarg_size 40
		.amdhsa_user_sgpr_count 12
		.amdhsa_user_sgpr_dispatch_ptr 0
		.amdhsa_user_sgpr_queue_ptr 0
		.amdhsa_user_sgpr_kernarg_segment_ptr 1
		.amdhsa_user_sgpr_dispatch_id 0
		.amdhsa_user_sgpr_kernarg_preload_length 10
		.amdhsa_user_sgpr_kernarg_preload_offset 0
		.amdhsa_user_sgpr_private_segment_size 0
		.amdhsa_uses_dynamic_stack 0
		.amdhsa_enable_private_segment 0
		.amdhsa_system_sgpr_workgroup_id_x 1
		.amdhsa_system_sgpr_workgroup_id_y 0
		.amdhsa_system_sgpr_workgroup_id_z 0
		.amdhsa_system_sgpr_workgroup_info 0
		.amdhsa_system_vgpr_workitem_id 0
		.amdhsa_next_free_vgpr 232
		.amdhsa_next_free_sgpr 96
		.amdhsa_accum_offset 232
		.amdhsa_reserve_vcc 1
		.amdhsa_float_round_mode_32 0
		.amdhsa_float_round_mode_16_64 0
		.amdhsa_float_denorm_mode_32 3
		.amdhsa_float_denorm_mode_16_64 3
		.amdhsa_dx10_clamp 1
		.amdhsa_ieee_mode 1
		.amdhsa_fp16_overflow 0
		.amdhsa_tg_split 0
		.amdhsa_exception_fp_ieee_invalid_op 0
		.amdhsa_exception_fp_denorm_src 0
		.amdhsa_exception_fp_ieee_div_zero 0
		.amdhsa_exception_fp_ieee_overflow 0
		.amdhsa_exception_fp_ieee_underflow 0
		.amdhsa_exception_fp_ieee_inexact 0
		.amdhsa_exception_int_div_zero 0
	.end_amdhsa_kernel
